# combine: next-layer gain loaded once per phase (was 2 load+drain per row); router row pass: the wave's 8 x rows prefetched before the top-4 selection into a register queue
# speedup vs baseline: 1.0181x; 1.0007x over previous
.LBB0_1741:
	s_mov_b32 s72, s73
	v_readlane_b32 s2, v254, 4
	v_readlane_b32 s1, v254, 2
	s_mov_b32 s4, 2
	v_readlane_b32 s1, v254, 3
	v_readlane_b32 s0, v255, 4
	s_ashr_i32 s5, s4, 31
	s_lshl_b32 s0, s0, 10
	s_lshl_b64 s[4:5], s[4:5], 3
	s_add_u32 s4, s94, s4
	s_addc_u32 s5, s95, s5
	s_load_dwordx2 s[4:5], s[4:5], 0x0
	s_mov_b32 s1, s73
	s_lshl_b64 s[76:77], s[0:1], 2
	s_mov_b32 s0, 18
	s_waitcnt lgkmcnt(0)
	s_add_u32 s4, s4, s76
	s_addc_u32 s5, s5, s77
	s_ashr_i32 s1, s0, 31
	s_lshl_b64 s[0:1], s[0:1], 3
	s_add_u32 s0, s94, s0
	s_addc_u32 s1, s95, s1
	s_load_dwordx2 s[8:9], s[0:1], 0x0
	s_mov_b32 s0, 19
	v_mov_b32_e32 v19, v0
	s_ashr_i32 s1, s0, 31
	v_and_b32_e32 v112, 63, v19
	v_lshlrev_b32_e32 v1, 6, v112
	global_load_dwordx4 v[4:7], v1, s[4:5] offset:48
	global_load_dwordx4 v[8:11], v1, s[4:5] offset:32
	global_load_dwordx4 v[12:15], v1, s[4:5] offset:16
	global_load_dwordx4 v[36:39], v1, s[4:5]
	s_lshl_b64 s[0:1], s[0:1], 3
	s_add_u32 s0, s94, s0
	s_addc_u32 s1, s95, s1
	v_readfirstlane_b32 s3, v19
	v_cmp_gt_i32_e64 s[6:7], 32, v19
	v_lshl_add_u32 v113, v19, 2, 0
	s_and_saveexec_b64 s[10:11], s[6:7]
	v_add_u32_e32 v1, 0x22500, v113
	ds_write_b32 v1, v3
	s_or_b64 exec, exec, s[10:11]
	v_readlane_b32 s10, v255, 4
	v_readlane_b32 s12, v254, 15
	s_lshl_b32 s10, s10, 15
	v_readlane_b32 s14, v254, 17
	s_mov_b32 s11, s73
	v_readlane_b32 s15, v254, 18
	s_add_u32 s80, s14, s72
	s_addc_u32 s81, s15, 0
	s_lshl_b64 s[10:11], s[10:11], 2
	s_waitcnt lgkmcnt(0)
	s_add_u32 s8, s8, s10
	s_addc_u32 s9, s9, s11
	s_ashr_i32 s89, s3, 6
	v_lshrrev_b32_e32 v1, 5, v112
	s_lshl_b32 s78, s89, 7
	v_lshl_or_b32 v30, v1, 3, s78
	v_and_b32_e32 v114, 31, v19
	v_or_b32_e32 v34, 1, v30
	v_lshlrev_b32_e32 v2, 2, v114
	v_ashrrev_i32_e32 v31, 31, v30
	v_ashrrev_i32_e32 v35, 31, v34
	v_lshl_add_u64 v[28:29], s[8:9], 0, v[2:3]
	s_waitcnt vmcnt(4)
	v_lshlrev_b64 v[20:21], 7, v[30:31]
	v_lshlrev_b64 v[34:35], 7, v[34:35]
	v_lshl_add_u64 v[20:21], v[28:29], 0, v[20:21]
	v_lshl_add_u64 v[32:33], v[30:31], 2, s[4:5]
	v_lshl_add_u64 v[34:35], v[28:29], 0, v[34:35]
	s_load_dwordx2 s[0:1], s[0:1], 0x0
	v_lshlrev_b32_e32 v108, 4, v1
	global_load_dword v1, v[20:21], off
	s_nop 0
	global_load_dwordx4 v[20:23], v[32:33], off offset:16
	global_load_dwordx4 v[24:27], v[32:33], off
	global_load_dword v41, v[34:35], off
	v_or_b32_e32 v34, 2, v30
	v_ashrrev_i32_e32 v35, 31, v34
	v_lshlrev_b64 v[34:35], 7, v[34:35]
	v_lshl_add_u64 v[34:35], v[28:29], 0, v[34:35]
	global_load_dword v42, v[34:35], off
	v_or_b32_e32 v34, 3, v30
	v_ashrrev_i32_e32 v35, 31, v34
	v_lshlrev_b64 v[34:35], 7, v[34:35]
	v_lshl_add_u64 v[34:35], v[28:29], 0, v[34:35]
	global_load_dword v45, v[34:35], off
	v_or_b32_e32 v34, 4, v30
	v_ashrrev_i32_e32 v35, 31, v34
	v_lshlrev_b64 v[34:35], 7, v[34:35]
	v_lshl_add_u64 v[34:35], v[28:29], 0, v[34:35]
	global_load_dword v47, v[34:35], off
	v_or_b32_e32 v34, 5, v30
	v_ashrrev_i32_e32 v35, 31, v34
	v_lshlrev_b64 v[34:35], 7, v[34:35]
	v_lshl_add_u64 v[34:35], v[28:29], 0, v[34:35]
	global_load_dword v49, v[34:35], off
	v_or_b32_e32 v34, 6, v30
	v_ashrrev_i32_e32 v35, 31, v34
	v_lshlrev_b64 v[34:35], 7, v[34:35]
	v_lshl_add_u64 v[34:35], v[28:29], 0, v[34:35]
	global_load_dword v51, v[34:35], off
	v_or_b32_e32 v34, 7, v30
	v_ashrrev_i32_e32 v35, 31, v34
	v_lshlrev_b64 v[34:35], 7, v[34:35]
	v_lshl_add_u64 v[34:35], v[28:29], 0, v[34:35]
	global_load_dword v34, v[34:35], off
	s_ashr_i32 s79, s78, 31
	s_lshl_b32 s88, s2, 6
	s_lshl_b64 s[8:9], s[78:79], 1
	s_add_u32 s8, s80, s8
	s_addc_u32 s9, s81, s9
	v_mov_b32_e32 v109, v3
	v_or_b32_e32 v110, s88, v114
	v_lshl_add_u64 v[16:17], s[8:9], 0, v[108:109]
	s_mov_b64 s[8:9], 0xc9000000
	v_ashrrev_i32_e32 v111, 31, v110
	v_lshl_add_u64 v[16:17], v[16:17], 0, s[8:9]
	s_and_b32 s8, s3, 0xffffffc0
	s_lshl_b32 s2, s8, 2
	s_add_i32 s2, s2, 0
	s_add_i32 s2, s2, 0x10800
	v_cmp_gt_u32_e32 vcc, 32, v112
	v_add_u32_e32 v2, s2, v2
	v_readlane_b32 s13, v254, 16
	s_waitcnt vmcnt(7)
	v_mul_f32_e32 v31, v1, v24
	s_waitcnt vmcnt(6)
	v_mul_f32_e32 v40, v41, v25
	v_cvt_pk_bf16_f32 v40, v31, v40
	s_waitcnt vmcnt(5)
	v_mul_f32_e32 v43, v42, v26
	v_lshlrev_b32_e32 v31, 16, v40
	v_fma_f32 v1, v1, v24, -v31
	v_and_b32_e32 v24, 0xffff0000, v40
	v_fma_f32 v24, v41, v25, -v24
	s_waitcnt vmcnt(4)
	v_mul_f32_e32 v46, v45, v27
	v_cvt_pk_bf16_f32 v44, v1, v24
	v_cvt_pk_bf16_f32 v41, v43, v46
	s_waitcnt vmcnt(3)
	v_mul_f32_e32 v48, v47, v20
	v_lshlrev_b32_e32 v1, 16, v41
	v_fma_f32 v1, v42, v26, -v1
	v_and_b32_e32 v24, 0xffff0000, v41
	v_fma_f32 v24, v45, v27, -v24
	s_waitcnt vmcnt(2)
	v_mul_f32_e32 v50, v49, v21
	v_cvt_pk_bf16_f32 v45, v1, v24
	v_cvt_pk_bf16_f32 v42, v48, v50
	s_waitcnt vmcnt(1)
	v_mul_f32_e32 v52, v51, v22
	v_lshlrev_b32_e32 v1, 16, v42
	v_fma_f32 v1, v47, v20, -v1
	v_and_b32_e32 v20, 0xffff0000, v42
	v_fma_f32 v20, v49, v21, -v20
	s_waitcnt vmcnt(0)
	v_mul_f32_e32 v35, v34, v23
	v_cvt_pk_bf16_f32 v46, v1, v20
	v_cvt_pk_bf16_f32 v43, v52, v35
	s_nop 0
	v_and_b32_e32 v20, 0xffff0000, v43
	v_lshlrev_b32_e32 v1, 16, v43
	v_fma_f32 v20, v34, v23, -v20
	v_fma_f32 v1, v51, v22, -v1
	v_cvt_pk_bf16_f32 v47, v1, v20
	v_or_b32_e32 v20, 16, v30
	v_or_b32_e32 v34, 17, v30
	v_ashrrev_i32_e32 v21, 31, v20
	v_ashrrev_i32_e32 v35, 31, v34
	v_lshlrev_b64 v[20:21], 7, v[20:21]
	v_lshlrev_b64 v[34:35], 7, v[34:35]
	v_lshl_add_u64 v[20:21], v[28:29], 0, v[20:21]
	v_lshl_add_u64 v[34:35], v[28:29], 0, v[34:35]
	global_load_dword v1, v[20:21], off
	s_nop 0
	global_load_dwordx4 v[20:23], v[32:33], off offset:80
	global_load_dwordx4 v[24:27], v[32:33], off offset:64
	global_load_dword v49, v[34:35], off
	v_or_b32_e32 v34, 18, v30
	v_ashrrev_i32_e32 v35, 31, v34
	v_lshlrev_b64 v[34:35], 7, v[34:35]
	v_lshl_add_u64 v[34:35], v[28:29], 0, v[34:35]
	global_load_dword v50, v[34:35], off
	v_or_b32_e32 v34, 19, v30
	v_ashrrev_i32_e32 v35, 31, v34
	v_lshlrev_b64 v[34:35], 7, v[34:35]
	v_lshl_add_u64 v[34:35], v[28:29], 0, v[34:35]
	global_load_dword v53, v[34:35], off
	v_or_b32_e32 v34, 20, v30
	v_ashrrev_i32_e32 v35, 31, v34
	v_lshlrev_b64 v[34:35], 7, v[34:35]
	v_lshl_add_u64 v[34:35], v[28:29], 0, v[34:35]
	global_load_dword v55, v[34:35], off
	v_or_b32_e32 v34, 21, v30
	v_ashrrev_i32_e32 v35, 31, v34
	v_lshlrev_b64 v[34:35], 7, v[34:35]
	v_lshl_add_u64 v[34:35], v[28:29], 0, v[34:35]
	global_load_dword v57, v[34:35], off
	v_or_b32_e32 v34, 22, v30
	v_ashrrev_i32_e32 v35, 31, v34
	v_lshlrev_b64 v[34:35], 7, v[34:35]
	v_lshl_add_u64 v[34:35], v[28:29], 0, v[34:35]
	global_load_dword v59, v[34:35], off
	v_or_b32_e32 v34, 23, v30
	v_ashrrev_i32_e32 v35, 31, v34
	v_lshlrev_b64 v[34:35], 7, v[34:35]
	v_lshl_add_u64 v[34:35], v[28:29], 0, v[34:35]
	global_load_dword v34, v[34:35], off
	s_waitcnt vmcnt(7)
	v_mul_f32_e32 v31, v1, v24
	s_waitcnt vmcnt(6)
	v_mul_f32_e32 v48, v49, v25
	v_cvt_pk_bf16_f32 v48, v31, v48
	s_waitcnt vmcnt(5)
	v_mul_f32_e32 v51, v50, v26
	v_lshlrev_b32_e32 v31, 16, v48
	v_fma_f32 v1, v1, v24, -v31
	v_and_b32_e32 v24, 0xffff0000, v48
	v_fma_f32 v24, v49, v25, -v24
	s_waitcnt vmcnt(4)
	v_mul_f32_e32 v54, v53, v27
	v_cvt_pk_bf16_f32 v52, v1, v24
	v_cvt_pk_bf16_f32 v49, v51, v54
	s_waitcnt vmcnt(3)
	v_mul_f32_e32 v56, v55, v20
	v_lshlrev_b32_e32 v1, 16, v49
	v_fma_f32 v1, v50, v26, -v1
	v_and_b32_e32 v24, 0xffff0000, v49
	v_fma_f32 v24, v53, v27, -v24
	s_waitcnt vmcnt(2)
	v_mul_f32_e32 v58, v57, v21
	v_cvt_pk_bf16_f32 v53, v1, v24
	v_cvt_pk_bf16_f32 v50, v56, v58
	s_waitcnt vmcnt(1)
	v_mul_f32_e32 v60, v59, v22
	v_lshlrev_b32_e32 v1, 16, v50
	v_fma_f32 v1, v55, v20, -v1
	v_and_b32_e32 v20, 0xffff0000, v50
	v_fma_f32 v20, v57, v21, -v20
	s_waitcnt vmcnt(0)
	v_mul_f32_e32 v35, v34, v23
	v_cvt_pk_bf16_f32 v54, v1, v20
	v_cvt_pk_bf16_f32 v51, v60, v35
	s_nop 0
	v_and_b32_e32 v20, 0xffff0000, v51
	v_lshlrev_b32_e32 v1, 16, v51
	v_fma_f32 v20, v34, v23, -v20
	v_fma_f32 v1, v59, v22, -v1
	v_cvt_pk_bf16_f32 v55, v1, v20
	v_or_b32_e32 v20, 32, v30
	v_or_b32_e32 v34, 33, v30
	v_ashrrev_i32_e32 v21, 31, v20
	v_ashrrev_i32_e32 v35, 31, v34
	v_lshlrev_b64 v[20:21], 7, v[20:21]
	v_lshlrev_b64 v[34:35], 7, v[34:35]
	v_lshl_add_u64 v[20:21], v[28:29], 0, v[20:21]
	v_lshl_add_u64 v[34:35], v[28:29], 0, v[34:35]
	global_load_dword v1, v[20:21], off
	s_nop 0
	global_load_dwordx4 v[20:23], v[32:33], off offset:144
	global_load_dwordx4 v[24:27], v[32:33], off offset:128
	global_load_dword v57, v[34:35], off
	v_or_b32_e32 v34, 34, v30
	v_ashrrev_i32_e32 v35, 31, v34
	v_lshlrev_b64 v[34:35], 7, v[34:35]
	v_lshl_add_u64 v[34:35], v[28:29], 0, v[34:35]
	global_load_dword v58, v[34:35], off
	v_or_b32_e32 v34, 35, v30
	v_ashrrev_i32_e32 v35, 31, v34
	v_lshlrev_b64 v[34:35], 7, v[34:35]
	v_lshl_add_u64 v[34:35], v[28:29], 0, v[34:35]
	global_load_dword v61, v[34:35], off
	v_or_b32_e32 v34, 36, v30
	v_ashrrev_i32_e32 v35, 31, v34
	v_lshlrev_b64 v[34:35], 7, v[34:35]
	v_lshl_add_u64 v[34:35], v[28:29], 0, v[34:35]
	global_load_dword v63, v[34:35], off
	v_or_b32_e32 v34, 37, v30
	v_ashrrev_i32_e32 v35, 31, v34
	v_lshlrev_b64 v[34:35], 7, v[34:35]
	v_lshl_add_u64 v[34:35], v[28:29], 0, v[34:35]
	global_load_dword v65, v[34:35], off
	v_or_b32_e32 v34, 38, v30
	v_ashrrev_i32_e32 v35, 31, v34
	v_lshlrev_b64 v[34:35], 7, v[34:35]
	v_lshl_add_u64 v[34:35], v[28:29], 0, v[34:35]
	global_load_dword v67, v[34:35], off
	v_or_b32_e32 v34, 39, v30
	v_ashrrev_i32_e32 v35, 31, v34
	v_lshlrev_b64 v[34:35], 7, v[34:35]
	v_lshl_add_u64 v[34:35], v[28:29], 0, v[34:35]
	global_load_dword v34, v[34:35], off
	s_waitcnt vmcnt(7)
	v_mul_f32_e32 v31, v1, v24
	s_waitcnt vmcnt(6)
	v_mul_f32_e32 v56, v57, v25
	v_cvt_pk_bf16_f32 v56, v31, v56
	s_waitcnt vmcnt(5)
	v_mul_f32_e32 v59, v58, v26
	v_lshlrev_b32_e32 v31, 16, v56
	v_fma_f32 v1, v1, v24, -v31
	v_and_b32_e32 v24, 0xffff0000, v56
	v_fma_f32 v24, v57, v25, -v24
	s_waitcnt vmcnt(4)
	v_mul_f32_e32 v62, v61, v27
	v_cvt_pk_bf16_f32 v60, v1, v24
	v_cvt_pk_bf16_f32 v57, v59, v62
	s_waitcnt vmcnt(3)
	v_mul_f32_e32 v64, v63, v20
	v_lshlrev_b32_e32 v1, 16, v57
	v_fma_f32 v1, v58, v26, -v1
	v_and_b32_e32 v24, 0xffff0000, v57
	v_fma_f32 v24, v61, v27, -v24
	s_waitcnt vmcnt(2)
	v_mul_f32_e32 v66, v65, v21
	v_cvt_pk_bf16_f32 v61, v1, v24
	v_cvt_pk_bf16_f32 v58, v64, v66
	s_waitcnt vmcnt(1)
	v_mul_f32_e32 v68, v67, v22
	v_lshlrev_b32_e32 v1, 16, v58
	v_fma_f32 v1, v63, v20, -v1
	v_and_b32_e32 v20, 0xffff0000, v58
	v_fma_f32 v20, v65, v21, -v20
	s_waitcnt vmcnt(0)
	v_mul_f32_e32 v35, v34, v23
	v_cvt_pk_bf16_f32 v62, v1, v20
	v_cvt_pk_bf16_f32 v59, v68, v35
	s_nop 0
	v_and_b32_e32 v20, 0xffff0000, v59
	v_lshlrev_b32_e32 v1, 16, v59
	v_fma_f32 v20, v34, v23, -v20
	v_fma_f32 v1, v67, v22, -v1
	v_cvt_pk_bf16_f32 v63, v1, v20
	v_or_b32_e32 v20, 48, v30
	v_or_b32_e32 v34, 49, v30
	v_ashrrev_i32_e32 v21, 31, v20
	v_ashrrev_i32_e32 v35, 31, v34
	v_lshlrev_b64 v[20:21], 7, v[20:21]
	v_lshlrev_b64 v[34:35], 7, v[34:35]
	v_lshl_add_u64 v[20:21], v[28:29], 0, v[20:21]
	v_lshl_add_u64 v[34:35], v[28:29], 0, v[34:35]
	global_load_dword v1, v[20:21], off
	s_nop 0
	global_load_dwordx4 v[20:23], v[32:33], off offset:208
	global_load_dwordx4 v[24:27], v[32:33], off offset:192
	global_load_dword v65, v[34:35], off
	v_or_b32_e32 v34, 50, v30
	v_ashrrev_i32_e32 v35, 31, v34
	v_lshlrev_b64 v[34:35], 7, v[34:35]
	v_lshl_add_u64 v[34:35], v[28:29], 0, v[34:35]
	global_load_dword v66, v[34:35], off
	v_or_b32_e32 v34, 51, v30
	v_ashrrev_i32_e32 v35, 31, v34
	v_lshlrev_b64 v[34:35], 7, v[34:35]
	v_lshl_add_u64 v[34:35], v[28:29], 0, v[34:35]
	global_load_dword v69, v[34:35], off
	v_or_b32_e32 v34, 52, v30
	v_ashrrev_i32_e32 v35, 31, v34
	v_lshlrev_b64 v[34:35], 7, v[34:35]
	v_lshl_add_u64 v[34:35], v[28:29], 0, v[34:35]
	global_load_dword v71, v[34:35], off
	v_or_b32_e32 v34, 53, v30
	v_ashrrev_i32_e32 v35, 31, v34
	v_lshlrev_b64 v[34:35], 7, v[34:35]
	v_lshl_add_u64 v[34:35], v[28:29], 0, v[34:35]
	global_load_dword v73, v[34:35], off
	v_or_b32_e32 v34, 54, v30
	v_ashrrev_i32_e32 v35, 31, v34
	v_lshlrev_b64 v[34:35], 7, v[34:35]
	v_lshl_add_u64 v[34:35], v[28:29], 0, v[34:35]
	global_load_dword v75, v[34:35], off
	v_or_b32_e32 v34, 55, v30
	v_ashrrev_i32_e32 v35, 31, v34
	v_lshlrev_b64 v[34:35], 7, v[34:35]
	v_lshl_add_u64 v[34:35], v[28:29], 0, v[34:35]
	global_load_dword v34, v[34:35], off
	s_waitcnt vmcnt(7)
	v_mul_f32_e32 v31, v1, v24
	s_waitcnt vmcnt(6)
	v_mul_f32_e32 v64, v65, v25
	v_cvt_pk_bf16_f32 v64, v31, v64
	s_waitcnt vmcnt(5)
	v_mul_f32_e32 v67, v66, v26
	v_lshlrev_b32_e32 v31, 16, v64
	v_fma_f32 v1, v1, v24, -v31
	v_and_b32_e32 v24, 0xffff0000, v64
	v_fma_f32 v24, v65, v25, -v24
	s_waitcnt vmcnt(4)
	v_mul_f32_e32 v70, v69, v27
	v_cvt_pk_bf16_f32 v68, v1, v24
	v_cvt_pk_bf16_f32 v65, v67, v70
	s_waitcnt vmcnt(3)
	v_mul_f32_e32 v72, v71, v20
	v_lshlrev_b32_e32 v1, 16, v65
	v_fma_f32 v1, v66, v26, -v1
	v_and_b32_e32 v24, 0xffff0000, v65
	v_fma_f32 v24, v69, v27, -v24
	s_waitcnt vmcnt(2)
	v_mul_f32_e32 v74, v73, v21
	v_cvt_pk_bf16_f32 v69, v1, v24
	v_cvt_pk_bf16_f32 v66, v72, v74
	s_waitcnt vmcnt(1)
	v_mul_f32_e32 v76, v75, v22
	v_lshlrev_b32_e32 v1, 16, v66
	v_fma_f32 v1, v71, v20, -v1
	v_and_b32_e32 v20, 0xffff0000, v66
	v_fma_f32 v20, v73, v21, -v20
	s_waitcnt vmcnt(0)
	v_mul_f32_e32 v35, v34, v23
	v_cvt_pk_bf16_f32 v70, v1, v20
	v_cvt_pk_bf16_f32 v67, v76, v35
	s_nop 0
	v_and_b32_e32 v20, 0xffff0000, v67
	v_lshlrev_b32_e32 v1, 16, v67
	v_fma_f32 v20, v34, v23, -v20
	v_fma_f32 v1, v75, v22, -v1
	v_cvt_pk_bf16_f32 v71, v1, v20
	v_or_b32_e32 v20, 64, v30
	v_or_b32_e32 v34, 0x41, v30
	v_ashrrev_i32_e32 v21, 31, v20
	v_ashrrev_i32_e32 v35, 31, v34
	v_lshlrev_b64 v[20:21], 7, v[20:21]
	v_lshlrev_b64 v[34:35], 7, v[34:35]
	v_lshl_add_u64 v[20:21], v[28:29], 0, v[20:21]
	v_lshl_add_u64 v[34:35], v[28:29], 0, v[34:35]
	global_load_dword v1, v[20:21], off
	s_nop 0
	global_load_dwordx4 v[20:23], v[32:33], off offset:272
	global_load_dwordx4 v[24:27], v[32:33], off offset:256
	global_load_dword v73, v[34:35], off
	v_or_b32_e32 v34, 0x42, v30
	v_ashrrev_i32_e32 v35, 31, v34
	v_lshlrev_b64 v[34:35], 7, v[34:35]
	v_lshl_add_u64 v[34:35], v[28:29], 0, v[34:35]
	global_load_dword v74, v[34:35], off
	v_or_b32_e32 v34, 0x43, v30
	v_ashrrev_i32_e32 v35, 31, v34
	v_lshlrev_b64 v[34:35], 7, v[34:35]
	v_lshl_add_u64 v[34:35], v[28:29], 0, v[34:35]
	global_load_dword v77, v[34:35], off
	v_or_b32_e32 v34, 0x44, v30
	v_ashrrev_i32_e32 v35, 31, v34
	v_lshlrev_b64 v[34:35], 7, v[34:35]
	v_lshl_add_u64 v[34:35], v[28:29], 0, v[34:35]
	global_load_dword v79, v[34:35], off
	v_or_b32_e32 v34, 0x45, v30
	v_ashrrev_i32_e32 v35, 31, v34
	v_lshlrev_b64 v[34:35], 7, v[34:35]
	v_lshl_add_u64 v[34:35], v[28:29], 0, v[34:35]
	global_load_dword v81, v[34:35], off
	v_or_b32_e32 v34, 0x46, v30
	v_ashrrev_i32_e32 v35, 31, v34
	v_lshlrev_b64 v[34:35], 7, v[34:35]
	v_lshl_add_u64 v[34:35], v[28:29], 0, v[34:35]
	global_load_dword v83, v[34:35], off
	v_or_b32_e32 v34, 0x47, v30
	v_ashrrev_i32_e32 v35, 31, v34
	v_lshlrev_b64 v[34:35], 7, v[34:35]
	v_lshl_add_u64 v[34:35], v[28:29], 0, v[34:35]
	global_load_dword v34, v[34:35], off
	s_waitcnt vmcnt(7)
	v_mul_f32_e32 v31, v1, v24
	s_waitcnt vmcnt(6)
	v_mul_f32_e32 v72, v73, v25
	v_cvt_pk_bf16_f32 v72, v31, v72
	s_waitcnt vmcnt(5)
	v_mul_f32_e32 v75, v74, v26
	v_lshlrev_b32_e32 v31, 16, v72
	v_fma_f32 v1, v1, v24, -v31
	v_and_b32_e32 v24, 0xffff0000, v72
	v_fma_f32 v24, v73, v25, -v24
	s_waitcnt vmcnt(4)
	v_mul_f32_e32 v78, v77, v27
	v_cvt_pk_bf16_f32 v76, v1, v24
	v_cvt_pk_bf16_f32 v73, v75, v78
	s_waitcnt vmcnt(3)
	v_mul_f32_e32 v80, v79, v20
	v_lshlrev_b32_e32 v1, 16, v73
	v_fma_f32 v1, v74, v26, -v1
	v_and_b32_e32 v24, 0xffff0000, v73
	v_fma_f32 v24, v77, v27, -v24
	s_waitcnt vmcnt(2)
	v_mul_f32_e32 v82, v81, v21
	v_cvt_pk_bf16_f32 v77, v1, v24
	v_cvt_pk_bf16_f32 v74, v80, v82
	s_waitcnt vmcnt(1)
	v_mul_f32_e32 v84, v83, v22
	v_lshlrev_b32_e32 v1, 16, v74
	v_fma_f32 v1, v79, v20, -v1
	v_and_b32_e32 v20, 0xffff0000, v74
	v_fma_f32 v20, v81, v21, -v20
	s_waitcnt vmcnt(0)
	v_mul_f32_e32 v35, v34, v23
	v_cvt_pk_bf16_f32 v78, v1, v20
	v_cvt_pk_bf16_f32 v75, v84, v35
	s_nop 0
	v_and_b32_e32 v20, 0xffff0000, v75
	v_lshlrev_b32_e32 v1, 16, v75
	v_fma_f32 v20, v34, v23, -v20
	v_fma_f32 v1, v83, v22, -v1
	v_cvt_pk_bf16_f32 v79, v1, v20
	v_or_b32_e32 v20, 0x50, v30
	v_or_b32_e32 v34, 0x51, v30
	v_ashrrev_i32_e32 v21, 31, v20
	v_ashrrev_i32_e32 v35, 31, v34
	v_lshlrev_b64 v[20:21], 7, v[20:21]
	v_lshlrev_b64 v[34:35], 7, v[34:35]
	v_lshl_add_u64 v[20:21], v[28:29], 0, v[20:21]
	v_lshl_add_u64 v[34:35], v[28:29], 0, v[34:35]
	global_load_dword v1, v[20:21], off
	s_nop 0
	global_load_dwordx4 v[20:23], v[32:33], off offset:336
	global_load_dwordx4 v[24:27], v[32:33], off offset:320
	global_load_dword v81, v[34:35], off
	v_or_b32_e32 v34, 0x52, v30
	v_ashrrev_i32_e32 v35, 31, v34
	v_lshlrev_b64 v[34:35], 7, v[34:35]
	v_lshl_add_u64 v[34:35], v[28:29], 0, v[34:35]
	global_load_dword v82, v[34:35], off
	v_or_b32_e32 v34, 0x53, v30
	v_ashrrev_i32_e32 v35, 31, v34
	v_lshlrev_b64 v[34:35], 7, v[34:35]
	v_lshl_add_u64 v[34:35], v[28:29], 0, v[34:35]
	global_load_dword v85, v[34:35], off
	v_or_b32_e32 v34, 0x54, v30
	v_ashrrev_i32_e32 v35, 31, v34
	v_lshlrev_b64 v[34:35], 7, v[34:35]
	v_lshl_add_u64 v[34:35], v[28:29], 0, v[34:35]
	global_load_dword v87, v[34:35], off
	v_or_b32_e32 v34, 0x55, v30
	v_ashrrev_i32_e32 v35, 31, v34
	v_lshlrev_b64 v[34:35], 7, v[34:35]
	v_lshl_add_u64 v[34:35], v[28:29], 0, v[34:35]
	global_load_dword v89, v[34:35], off
	v_or_b32_e32 v34, 0x56, v30
	v_ashrrev_i32_e32 v35, 31, v34
	v_lshlrev_b64 v[34:35], 7, v[34:35]
	v_lshl_add_u64 v[34:35], v[28:29], 0, v[34:35]
	global_load_dword v91, v[34:35], off
	v_or_b32_e32 v34, 0x57, v30
	v_ashrrev_i32_e32 v35, 31, v34
	v_lshlrev_b64 v[34:35], 7, v[34:35]
	v_lshl_add_u64 v[34:35], v[28:29], 0, v[34:35]
	global_load_dword v34, v[34:35], off
	s_waitcnt vmcnt(7)
	v_mul_f32_e32 v31, v1, v24
	s_waitcnt vmcnt(6)
	v_mul_f32_e32 v80, v81, v25
	v_cvt_pk_bf16_f32 v80, v31, v80
	s_waitcnt vmcnt(5)
	v_mul_f32_e32 v83, v82, v26
	v_lshlrev_b32_e32 v31, 16, v80
	v_fma_f32 v1, v1, v24, -v31
	v_and_b32_e32 v24, 0xffff0000, v80
	v_fma_f32 v24, v81, v25, -v24
	s_waitcnt vmcnt(4)
	v_mul_f32_e32 v86, v85, v27
	v_cvt_pk_bf16_f32 v84, v1, v24
	v_cvt_pk_bf16_f32 v81, v83, v86
	s_waitcnt vmcnt(3)
	v_mul_f32_e32 v88, v87, v20
	v_lshlrev_b32_e32 v1, 16, v81
	v_fma_f32 v1, v82, v26, -v1
	v_and_b32_e32 v24, 0xffff0000, v81
	v_fma_f32 v24, v85, v27, -v24
	s_waitcnt vmcnt(2)
	v_mul_f32_e32 v90, v89, v21
	v_cvt_pk_bf16_f32 v85, v1, v24
	v_cvt_pk_bf16_f32 v82, v88, v90
	s_waitcnt vmcnt(1)
	v_mul_f32_e32 v92, v91, v22
	v_lshlrev_b32_e32 v1, 16, v82
	v_fma_f32 v1, v87, v20, -v1
	v_and_b32_e32 v20, 0xffff0000, v82
	v_fma_f32 v20, v89, v21, -v20
	s_waitcnt vmcnt(0)
	v_mul_f32_e32 v35, v34, v23
	v_cvt_pk_bf16_f32 v86, v1, v20
	v_cvt_pk_bf16_f32 v83, v92, v35
	s_nop 0
	v_and_b32_e32 v20, 0xffff0000, v83
	v_lshlrev_b32_e32 v1, 16, v83
	v_fma_f32 v20, v34, v23, -v20
	v_fma_f32 v1, v91, v22, -v1
	v_cvt_pk_bf16_f32 v87, v1, v20
	v_or_b32_e32 v20, 0x60, v30
	v_or_b32_e32 v34, 0x61, v30
	v_ashrrev_i32_e32 v21, 31, v20
	v_ashrrev_i32_e32 v35, 31, v34
	v_lshlrev_b64 v[20:21], 7, v[20:21]
	v_lshlrev_b64 v[34:35], 7, v[34:35]
	v_lshl_add_u64 v[20:21], v[28:29], 0, v[20:21]
	v_lshl_add_u64 v[34:35], v[28:29], 0, v[34:35]
	global_load_dword v1, v[20:21], off
	s_nop 0
	global_load_dwordx4 v[20:23], v[32:33], off offset:400
	global_load_dwordx4 v[24:27], v[32:33], off offset:384
	global_load_dword v88, v[34:35], off
	v_or_b32_e32 v34, 0x62, v30
	v_ashrrev_i32_e32 v35, 31, v34
	v_lshlrev_b64 v[34:35], 7, v[34:35]
	v_lshl_add_u64 v[34:35], v[28:29], 0, v[34:35]
	global_load_dword v90, v[34:35], off
	v_or_b32_e32 v34, 0x63, v30
	v_ashrrev_i32_e32 v35, 31, v34
	v_lshlrev_b64 v[34:35], 7, v[34:35]
	v_lshl_add_u64 v[34:35], v[28:29], 0, v[34:35]
	global_load_dword v92, v[34:35], off
	v_or_b32_e32 v34, 0x64, v30
	v_ashrrev_i32_e32 v35, 31, v34
	v_lshlrev_b64 v[34:35], 7, v[34:35]
	v_lshl_add_u64 v[34:35], v[28:29], 0, v[34:35]
	global_load_dword v94, v[34:35], off
	v_or_b32_e32 v34, 0x65, v30
	v_ashrrev_i32_e32 v35, 31, v34
	v_lshlrev_b64 v[34:35], 7, v[34:35]
	v_lshl_add_u64 v[34:35], v[28:29], 0, v[34:35]
	global_load_dword v99, v[34:35], off
	v_or_b32_e32 v34, 0x66, v30
	v_ashrrev_i32_e32 v35, 31, v34
	v_lshlrev_b64 v[34:35], 7, v[34:35]
	v_lshl_add_u64 v[34:35], v[28:29], 0, v[34:35]
	global_load_dword v103, v[34:35], off
	v_or_b32_e32 v34, 0x67, v30
	v_ashrrev_i32_e32 v35, 31, v34
	v_lshlrev_b64 v[34:35], 7, v[34:35]
	v_lshl_add_u64 v[34:35], v[28:29], 0, v[34:35]
	global_load_dword v34, v[34:35], off
	s_waitcnt vmcnt(7)
	v_mul_f32_e32 v31, v1, v24
	s_waitcnt vmcnt(6)
	v_mul_f32_e32 v89, v88, v25
	v_cvt_pk_bf16_f32 v96, v31, v89
	s_waitcnt vmcnt(5)
	v_mul_f32_e32 v91, v90, v26
	v_lshlrev_b32_e32 v31, 16, v96
	v_fma_f32 v1, v1, v24, -v31
	v_and_b32_e32 v24, 0xffff0000, v96
	v_fma_f32 v24, v88, v25, -v24
	s_waitcnt vmcnt(4)
	v_mul_f32_e32 v93, v92, v27
	v_cvt_pk_bf16_f32 v100, v1, v24
	v_cvt_pk_bf16_f32 v97, v91, v93
	s_waitcnt vmcnt(3)
	v_mul_f32_e32 v95, v94, v20
	v_lshlrev_b32_e32 v1, 16, v97
	v_fma_f32 v1, v90, v26, -v1
	v_and_b32_e32 v24, 0xffff0000, v97
	v_fma_f32 v24, v92, v27, -v24
	s_waitcnt vmcnt(2)
	v_mul_f32_e32 v98, v99, v21
	v_cvt_pk_bf16_f32 v101, v1, v24
	v_cvt_pk_bf16_f32 v98, v95, v98
	s_waitcnt vmcnt(1)
	v_mul_f32_e32 v104, v103, v22
	v_lshlrev_b32_e32 v1, 16, v98
	v_fma_f32 v1, v94, v20, -v1
	v_and_b32_e32 v20, 0xffff0000, v98
	v_fma_f32 v20, v99, v21, -v20
	s_waitcnt vmcnt(0)
	v_mul_f32_e32 v35, v34, v23
	v_cvt_pk_bf16_f32 v102, v1, v20
	v_cvt_pk_bf16_f32 v99, v104, v35
	s_nop 0
	v_and_b32_e32 v20, 0xffff0000, v99
	v_lshlrev_b32_e32 v1, 16, v99
	v_fma_f32 v20, v34, v23, -v20
	v_fma_f32 v1, v103, v22, -v1
	v_cvt_pk_bf16_f32 v103, v1, v20
	v_or_b32_e32 v20, 0x70, v30
	v_ashrrev_i32_e32 v21, 31, v20
	v_lshlrev_b64 v[20:21], 7, v[20:21]
	v_lshl_add_u64 v[20:21], v[28:29], 0, v[20:21]
	global_load_dword v1, v[20:21], off
	s_nop 0
	global_load_dwordx4 v[20:23], v[32:33], off offset:464
	global_load_dwordx4 v[24:27], v[32:33], off offset:448
	v_or_b32_e32 v32, 0x71, v30
	v_ashrrev_i32_e32 v33, 31, v32
	v_lshlrev_b64 v[32:33], 7, v[32:33]
	v_lshl_add_u64 v[32:33], v[28:29], 0, v[32:33]
	global_load_dword v35, v[32:33], off
	v_or_b32_e32 v32, 0x72, v30
	v_ashrrev_i32_e32 v33, 31, v32
	v_lshlrev_b64 v[32:33], 7, v[32:33]
	v_lshl_add_u64 v[32:33], v[28:29], 0, v[32:33]
	global_load_dword v89, v[32:33], off
	v_or_b32_e32 v32, 0x73, v30
	v_ashrrev_i32_e32 v33, 31, v32
	v_lshlrev_b64 v[32:33], 7, v[32:33]
	v_lshl_add_u64 v[32:33], v[28:29], 0, v[32:33]
	global_load_dword v91, v[32:33], off
	v_or_b32_e32 v32, 0x74, v30
	v_ashrrev_i32_e32 v33, 31, v32
	v_lshlrev_b64 v[32:33], 7, v[32:33]
	v_lshl_add_u64 v[32:33], v[28:29], 0, v[32:33]
	global_load_dword v95, v[32:33], off
	v_or_b32_e32 v32, 0x75, v30
	v_ashrrev_i32_e32 v33, 31, v32
	v_lshlrev_b64 v[32:33], 7, v[32:33]
	v_lshl_add_u64 v[32:33], v[28:29], 0, v[32:33]
	global_load_dword v104, v[32:33], off
	v_or_b32_e32 v32, 0x76, v30
	v_or_b32_e32 v30, 0x77, v30
	v_ashrrev_i32_e32 v33, 31, v32
	v_ashrrev_i32_e32 v31, 31, v30
	v_lshlrev_b64 v[32:33], 7, v[32:33]
	v_lshlrev_b64 v[30:31], 7, v[30:31]
	v_lshl_add_u64 v[32:33], v[28:29], 0, v[32:33]
	v_lshl_add_u64 v[28:29], v[28:29], 0, v[30:31]
	global_load_dword v32, v[32:33], off
	s_waitcnt vmcnt(6)
	v_mul_f32_e32 v34, v1, v24
	global_load_dword v28, v[28:29], off
	s_waitcnt vmcnt(6)
	v_mul_f32_e32 v88, v35, v25
	v_cvt_pk_bf16_f32 v92, v34, v88
	s_waitcnt vmcnt(5)
	v_mul_f32_e32 v90, v89, v26
	v_lshlrev_b32_e32 v30, 16, v92
	v_fma_f32 v1, v1, v24, -v30
	v_and_b32_e32 v24, 0xffff0000, v92
	v_fma_f32 v24, v35, v25, -v24
	s_waitcnt vmcnt(4)
	v_mul_f32_e32 v93, v91, v27
	v_cvt_pk_bf16_f32 v88, v1, v24
	v_cvt_pk_bf16_f32 v93, v90, v93
	s_waitcnt vmcnt(3)
	v_mul_f32_e32 v94, v95, v20
	v_lshlrev_b32_e32 v1, 16, v93
	v_fma_f32 v1, v89, v26, -v1
	v_and_b32_e32 v24, 0xffff0000, v93
	v_fma_f32 v24, v91, v27, -v24
	s_waitcnt vmcnt(2)
	v_mul_f32_e32 v105, v104, v21
	v_cvt_pk_bf16_f32 v89, v1, v24
	v_cvt_pk_bf16_f32 v94, v94, v105
	s_waitcnt vmcnt(1)
	v_mul_f32_e32 v33, v32, v22
	v_lshlrev_b32_e32 v1, 16, v94
	v_fma_f32 v1, v95, v20, -v1
	v_and_b32_e32 v20, 0xffff0000, v94
	v_fma_f32 v20, v104, v21, -v20
	v_cvt_pk_bf16_f32 v90, v1, v20
	s_waitcnt vmcnt(0)
	v_mul_f32_e32 v29, v28, v23
	v_cvt_pk_bf16_f32 v95, v33, v29
	s_nop 0
	v_and_b32_e32 v20, 0xffff0000, v95
	v_lshlrev_b32_e32 v1, 16, v95
	v_fma_f32 v20, v28, v23, -v20
	v_fma_f32 v1, v32, v22, -v1
	v_cvt_pk_bf16_f32 v91, v1, v20
	v_lshlrev_b64 v[20:21], 11, v[110:111]
	v_lshl_add_u64 v[104:105], v[16:17], 0, v[20:21]
	global_load_dwordx4 v[120:123], v[104:105], off
	global_load_dwordx4 v[124:127], v[104:105], off offset:32
	global_load_dwordx4 v[128:131], v[104:105], off offset:64
	global_load_dwordx4 v[132:135], v[104:105], off offset:96
	global_load_dwordx4 v[136:139], v[104:105], off offset:128
	global_load_dwordx4 v[140:143], v[104:105], off offset:160
	global_load_dwordx4 v[144:147], v[104:105], off offset:192
	global_load_dwordx4 v[148:151], v[104:105], off offset:224
	s_mov_b32 s100, 0x10000
	s_mov_b32 s101, 0
	v_lshl_add_u64 v[184:185], v[104:105], 0, s[100:101]
	global_load_dwordx4 v[152:155], v[184:185], off
	global_load_dwordx4 v[156:159], v[184:185], off offset:32
	global_load_dwordx4 v[160:163], v[184:185], off offset:64
	global_load_dwordx4 v[164:167], v[184:185], off offset:96
	global_load_dwordx4 v[168:171], v[184:185], off offset:128
	global_load_dwordx4 v[172:175], v[184:185], off offset:160
	global_load_dwordx4 v[176:179], v[184:185], off offset:192
	global_load_dwordx4 v[180:183], v[184:185], off offset:224
	s_waitcnt vmcnt(15)
	v_mov_b32_e32 v116, v120
	v_mov_b32_e32 v117, v121
	v_mov_b32_e32 v118, v122
	v_mov_b32_e32 v119, v123
	v_and_b32_e32 v20, 0xffff0000, v116
	v_lshlrev_b32_e32 v1, 16, v116
	v_mul_f32_e32 v20, v20, v20
	v_and_b32_e32 v21, 0xffff0000, v117
	v_fmac_f32_e32 v20, v1, v1
	v_lshlrev_b32_e32 v1, 16, v117
	v_mul_f32_e32 v21, v21, v21
	v_fmac_f32_e32 v21, v1, v1
	v_add_f32_e32 v1, v20, v21
	v_and_b32_e32 v21, 0xffff0000, v118
	v_lshlrev_b32_e32 v20, 16, v118
	v_mul_f32_e32 v21, v21, v21
	v_fmac_f32_e32 v21, v20, v20
	v_add_f32_e32 v1, v21, v1
	v_and_b32_e32 v21, 0xffff0000, v119
	v_lshlrev_b32_e32 v20, 16, v119
	v_mul_f32_e32 v21, v21, v21
	v_fmac_f32_e32 v21, v20, v20
	v_add_f32_e32 v1, v21, v1
	v_mfma_f32_32x32x16_bf16 v[20:35], v[40:43], v[116:119], 0
	v_mfma_f32_32x32x16_bf16 v[20:35], v[44:47], v[116:119], v[20:35]
	s_waitcnt vmcnt(14)
	v_mov_b32_e32 v116, v124
	v_mov_b32_e32 v117, v125
	v_mov_b32_e32 v118, v126
	v_mov_b32_e32 v119, v127
	v_and_b32_e32 v107, 0xffff0000, v116
	v_lshlrev_b32_e32 v106, 16, v116
	v_mul_f32_e32 v107, v107, v107
	v_mfma_f32_32x32x16_bf16 v[20:35], v[48:51], v[116:119], v[20:35]
	v_fmac_f32_e32 v107, v106, v106
	v_add_f32_e32 v1, v1, v107
	v_and_b32_e32 v107, 0xffff0000, v117
	v_lshlrev_b32_e32 v106, 16, v117
	v_mul_f32_e32 v107, v107, v107
	v_fmac_f32_e32 v107, v106, v106
	v_add_f32_e32 v1, v107, v1
	v_and_b32_e32 v107, 0xffff0000, v118
	v_lshlrev_b32_e32 v106, 16, v118
	v_mul_f32_e32 v107, v107, v107
	v_fmac_f32_e32 v107, v106, v106
	v_add_f32_e32 v1, v107, v1
	v_lshlrev_b32_e32 v106, 16, v119
	v_and_b32_e32 v107, 0xffff0000, v119
	v_mfma_f32_32x32x16_bf16 v[20:35], v[52:55], v[116:119], v[20:35]
	v_mul_f32_e32 v107, v107, v107
	v_fmac_f32_e32 v107, v106, v106
	v_add_f32_e32 v1, v107, v1
	s_waitcnt vmcnt(13)
	v_mov_b32_e32 v116, v128
	v_mov_b32_e32 v117, v129
	v_mov_b32_e32 v118, v130
	v_mov_b32_e32 v119, v131
	v_and_b32_e32 v107, 0xffff0000, v116
	v_lshlrev_b32_e32 v106, 16, v116
	v_mul_f32_e32 v107, v107, v107
	v_mfma_f32_32x32x16_bf16 v[20:35], v[56:59], v[116:119], v[20:35]
	v_fmac_f32_e32 v107, v106, v106
	v_add_f32_e32 v1, v107, v1
	v_and_b32_e32 v107, 0xffff0000, v117
	v_lshlrev_b32_e32 v106, 16, v117
	v_mul_f32_e32 v107, v107, v107
	v_fmac_f32_e32 v107, v106, v106
	v_add_f32_e32 v1, v107, v1
	v_and_b32_e32 v107, 0xffff0000, v118
	v_lshlrev_b32_e32 v106, 16, v118
	v_mul_f32_e32 v107, v107, v107
	v_fmac_f32_e32 v107, v106, v106
	v_add_f32_e32 v1, v107, v1
	v_lshlrev_b32_e32 v106, 16, v119
	v_and_b32_e32 v107, 0xffff0000, v119
	v_mfma_f32_32x32x16_bf16 v[20:35], v[60:63], v[116:119], v[20:35]
	v_mul_f32_e32 v107, v107, v107
	v_fmac_f32_e32 v107, v106, v106
	v_add_f32_e32 v1, v107, v1
	s_waitcnt vmcnt(12)
	v_mov_b32_e32 v116, v132
	v_mov_b32_e32 v117, v133
	v_mov_b32_e32 v118, v134
	v_mov_b32_e32 v119, v135
	v_and_b32_e32 v107, 0xffff0000, v116
	v_lshlrev_b32_e32 v106, 16, v116
	v_mul_f32_e32 v107, v107, v107
	v_mfma_f32_32x32x16_bf16 v[20:35], v[64:67], v[116:119], v[20:35]
	v_fmac_f32_e32 v107, v106, v106
	v_add_f32_e32 v1, v107, v1
	v_and_b32_e32 v107, 0xffff0000, v117
	v_lshlrev_b32_e32 v106, 16, v117
	v_mul_f32_e32 v107, v107, v107
	v_fmac_f32_e32 v107, v106, v106
	v_add_f32_e32 v1, v107, v1
	v_and_b32_e32 v107, 0xffff0000, v118
	v_lshlrev_b32_e32 v106, 16, v118
	v_mul_f32_e32 v107, v107, v107
	v_fmac_f32_e32 v107, v106, v106
	v_add_f32_e32 v1, v107, v1
	v_lshlrev_b32_e32 v106, 16, v119
	v_and_b32_e32 v107, 0xffff0000, v119
	v_mfma_f32_32x32x16_bf16 v[20:35], v[68:71], v[116:119], v[20:35]
	v_mul_f32_e32 v107, v107, v107
	v_fmac_f32_e32 v107, v106, v106
	v_add_f32_e32 v1, v107, v1
	s_waitcnt vmcnt(11)
	v_mov_b32_e32 v116, v136
	v_mov_b32_e32 v117, v137
	v_mov_b32_e32 v118, v138
	v_mov_b32_e32 v119, v139
	v_and_b32_e32 v107, 0xffff0000, v116
	v_lshlrev_b32_e32 v106, 16, v116
	v_mul_f32_e32 v107, v107, v107
	v_mfma_f32_32x32x16_bf16 v[20:35], v[72:75], v[116:119], v[20:35]
	v_fmac_f32_e32 v107, v106, v106
	v_add_f32_e32 v1, v107, v1
	v_and_b32_e32 v107, 0xffff0000, v117
	v_lshlrev_b32_e32 v106, 16, v117
	v_mul_f32_e32 v107, v107, v107
	v_fmac_f32_e32 v107, v106, v106
	v_add_f32_e32 v1, v107, v1
	v_and_b32_e32 v107, 0xffff0000, v118
	v_lshlrev_b32_e32 v106, 16, v118
	v_mul_f32_e32 v107, v107, v107
	v_fmac_f32_e32 v107, v106, v106
	v_add_f32_e32 v1, v107, v1
	v_lshlrev_b32_e32 v106, 16, v119
	v_and_b32_e32 v107, 0xffff0000, v119
	v_mfma_f32_32x32x16_bf16 v[20:35], v[76:79], v[116:119], v[20:35]
	v_mul_f32_e32 v107, v107, v107
	v_fmac_f32_e32 v107, v106, v106
	v_add_f32_e32 v1, v107, v1
	s_waitcnt vmcnt(10)
	v_mov_b32_e32 v116, v140
	v_mov_b32_e32 v117, v141
	v_mov_b32_e32 v118, v142
	v_mov_b32_e32 v119, v143
	v_and_b32_e32 v107, 0xffff0000, v116
	v_lshlrev_b32_e32 v106, 16, v116
	v_mul_f32_e32 v107, v107, v107
	v_mfma_f32_32x32x16_bf16 v[20:35], v[80:83], v[116:119], v[20:35]
	v_fmac_f32_e32 v107, v106, v106
	v_add_f32_e32 v1, v107, v1
	v_and_b32_e32 v107, 0xffff0000, v117
	v_lshlrev_b32_e32 v106, 16, v117
	v_mul_f32_e32 v107, v107, v107
	v_fmac_f32_e32 v107, v106, v106
	v_add_f32_e32 v1, v107, v1
	v_and_b32_e32 v107, 0xffff0000, v118
	v_lshlrev_b32_e32 v106, 16, v118
	v_mul_f32_e32 v107, v107, v107
	v_fmac_f32_e32 v107, v106, v106
	v_add_f32_e32 v1, v107, v1
	v_lshlrev_b32_e32 v106, 16, v119
	v_and_b32_e32 v107, 0xffff0000, v119
	v_mfma_f32_32x32x16_bf16 v[20:35], v[84:87], v[116:119], v[20:35]
	v_mul_f32_e32 v107, v107, v107
	v_fmac_f32_e32 v107, v106, v106
	v_add_f32_e32 v1, v107, v1
	s_waitcnt vmcnt(9)
	v_mov_b32_e32 v116, v144
	v_mov_b32_e32 v117, v145
	v_mov_b32_e32 v118, v146
	v_mov_b32_e32 v119, v147
	v_and_b32_e32 v107, 0xffff0000, v116
	v_lshlrev_b32_e32 v106, 16, v116
	v_mul_f32_e32 v107, v107, v107
	v_fmac_f32_e32 v107, v106, v106
	v_add_f32_e32 v1, v107, v1
	v_and_b32_e32 v107, 0xffff0000, v117
	v_lshlrev_b32_e32 v106, 16, v117
	v_mul_f32_e32 v107, v107, v107
	v_fmac_f32_e32 v107, v106, v106
	v_add_f32_e32 v1, v107, v1
	v_and_b32_e32 v107, 0xffff0000, v118
	v_lshlrev_b32_e32 v106, 16, v118
	v_mul_f32_e32 v107, v107, v107
	v_fmac_f32_e32 v107, v106, v106
	v_add_f32_e32 v1, v107, v1
	v_and_b32_e32 v107, 0xffff0000, v119
	v_lshlrev_b32_e32 v106, 16, v119
	v_mul_f32_e32 v107, v107, v107
	v_fmac_f32_e32 v107, v106, v106
	v_add_f32_e32 v109, v107, v1
	v_mfma_f32_32x32x16_bf16 v[20:35], v[96:99], v[116:119], v[20:35]
	s_waitcnt vmcnt(8)
	v_mov_b32_e32 v104, v148
	v_mov_b32_e32 v105, v149
	v_mov_b32_e32 v106, v150
	v_mov_b32_e32 v107, v151
	v_and_b32_e32 v111, 0xffff0000, v104
	v_mfma_f32_32x32x16_bf16 v[20:35], v[100:103], v[116:119], v[20:35]
	v_lshlrev_b32_e32 v1, 16, v104
	v_mul_f32_e32 v111, v111, v111
	v_fmac_f32_e32 v111, v1, v1
	v_add_f32_e32 v1, v111, v109
	v_and_b32_e32 v111, 0xffff0000, v105
	v_lshlrev_b32_e32 v109, 16, v105
	v_mul_f32_e32 v111, v111, v111
	v_mfma_f32_32x32x16_bf16 v[20:35], v[92:95], v[104:107], v[20:35]
	v_fmac_f32_e32 v111, v109, v109
	v_add_f32_e32 v1, v111, v1
	v_and_b32_e32 v111, 0xffff0000, v106
	v_lshlrev_b32_e32 v109, 16, v106
	v_mul_f32_e32 v111, v111, v111
	v_fmac_f32_e32 v111, v109, v109
	v_add_f32_e32 v1, v111, v1
	v_mfma_f32_32x32x16_bf16 v[20:35], v[88:91], v[104:107], v[20:35]
	v_and_b32_e32 v111, 0xffff0000, v107
	v_lshlrev_b32_e32 v109, 16, v107
	v_mul_f32_e32 v111, v111, v111
	v_fmac_f32_e32 v111, v109, v109
	v_add_f32_e32 v109, v111, v1
	v_mov_b32_e32 v104, v109
	s_nop 1
	v_permlane32_swap_b32_e32 v109, v104
	s_and_saveexec_b64 s[4:5], vcc
	v_add_f32_e32 v1, v109, v104
	ds_write_b32 v2, v1
	s_or_b64 exec, exec, s[4:5]
	v_or_b32_e32 v1, s8, v114
	s_movk_i32 s2, 0x84
	v_mul_lo_u32 v1, v1, s2
	v_add_u32_e32 v1, 0, v1
	v_add_u32_e32 v104, v1, v108
	ds_write2_b32 v104, v20, v21 offset1:1
	ds_write2_b32 v104, v22, v23 offset0:2 offset1:3
	ds_write2_b32 v104, v24, v25 offset0:8 offset1:9
	ds_write2_b32 v104, v26, v27 offset0:10 offset1:11
	ds_write2_b32 v104, v28, v29 offset0:16 offset1:17
	ds_write2_b32 v104, v30, v31 offset0:18 offset1:19
	ds_write2_b32 v104, v32, v33 offset0:24 offset1:25
	ds_write2_b32 v104, v34, v35 offset0:26 offset1:27
	v_or_b32_e32 v20, 32, v110
	v_ashrrev_i32_e32 v21, 31, v20
	v_lshlrev_b64 v[20:21], 11, v[20:21]
	v_lshl_add_u64 v[16:17], v[16:17], 0, v[20:21]
	s_waitcnt vmcnt(7)
	v_mov_b32_e32 v106, v152
	v_mov_b32_e32 v107, v153
	v_mov_b32_e32 v108, v154
	v_mov_b32_e32 v109, v155
	v_and_b32_e32 v20, 0xffff0000, v106
	v_lshlrev_b32_e32 v1, 16, v106
	v_mul_f32_e32 v20, v20, v20
	v_and_b32_e32 v21, 0xffff0000, v107
	v_fmac_f32_e32 v20, v1, v1
	v_lshlrev_b32_e32 v1, 16, v107
	v_mul_f32_e32 v21, v21, v21
	v_fmac_f32_e32 v21, v1, v1
	v_add_f32_e32 v1, v20, v21
	v_and_b32_e32 v21, 0xffff0000, v108
	v_lshlrev_b32_e32 v20, 16, v108
	v_mul_f32_e32 v21, v21, v21
	v_fmac_f32_e32 v21, v20, v20
	v_add_f32_e32 v1, v21, v1
	v_and_b32_e32 v21, 0xffff0000, v109
	v_lshlrev_b32_e32 v20, 16, v109
	v_mul_f32_e32 v21, v21, v21
	v_fmac_f32_e32 v21, v20, v20
	v_add_f32_e32 v1, v21, v1
	v_mfma_f32_32x32x16_bf16 v[20:35], v[40:43], v[106:109], 0
	v_mfma_f32_32x32x16_bf16 v[20:35], v[44:47], v[106:109], v[20:35]
	s_waitcnt vmcnt(6)
	v_mov_b32_e32 v40, v156
	v_mov_b32_e32 v41, v157
	v_mov_b32_e32 v42, v158
	v_mov_b32_e32 v43, v159
	v_and_b32_e32 v45, 0xffff0000, v40
	v_lshlrev_b32_e32 v44, 16, v40
	v_mul_f32_e32 v45, v45, v45
	v_mfma_f32_32x32x16_bf16 v[20:35], v[48:51], v[40:43], v[20:35]
	v_fmac_f32_e32 v45, v44, v44
	v_add_f32_e32 v1, v1, v45
	v_and_b32_e32 v45, 0xffff0000, v41
	v_lshlrev_b32_e32 v44, 16, v41
	v_mul_f32_e32 v45, v45, v45
	v_fmac_f32_e32 v45, v44, v44
	v_add_f32_e32 v1, v45, v1
	v_and_b32_e32 v45, 0xffff0000, v42
	v_lshlrev_b32_e32 v44, 16, v42
	v_mul_f32_e32 v45, v45, v45
	v_fmac_f32_e32 v45, v44, v44
	v_add_f32_e32 v1, v45, v1
	v_lshlrev_b32_e32 v44, 16, v43
	v_and_b32_e32 v45, 0xffff0000, v43
	v_mfma_f32_32x32x16_bf16 v[20:35], v[52:55], v[40:43], v[20:35]
	v_mul_f32_e32 v45, v45, v45
	v_fmac_f32_e32 v45, v44, v44
	v_add_f32_e32 v1, v45, v1
	s_waitcnt vmcnt(5)
	v_mov_b32_e32 v40, v160
	v_mov_b32_e32 v41, v161
	v_mov_b32_e32 v42, v162
	v_mov_b32_e32 v43, v163
	v_and_b32_e32 v45, 0xffff0000, v40
	v_lshlrev_b32_e32 v44, 16, v40
	v_mul_f32_e32 v45, v45, v45
	v_mfma_f32_32x32x16_bf16 v[20:35], v[56:59], v[40:43], v[20:35]
	v_fmac_f32_e32 v45, v44, v44
	v_add_f32_e32 v1, v45, v1
	v_and_b32_e32 v45, 0xffff0000, v41
	v_lshlrev_b32_e32 v44, 16, v41
	v_mul_f32_e32 v45, v45, v45
	v_fmac_f32_e32 v45, v44, v44
	v_add_f32_e32 v1, v45, v1
	v_and_b32_e32 v45, 0xffff0000, v42
	v_lshlrev_b32_e32 v44, 16, v42
	v_mul_f32_e32 v45, v45, v45
	v_fmac_f32_e32 v45, v44, v44
	v_add_f32_e32 v1, v45, v1
	v_lshlrev_b32_e32 v44, 16, v43
	v_and_b32_e32 v45, 0xffff0000, v43
	v_mfma_f32_32x32x16_bf16 v[20:35], v[60:63], v[40:43], v[20:35]
	v_mul_f32_e32 v45, v45, v45
	v_fmac_f32_e32 v45, v44, v44
	v_add_f32_e32 v1, v45, v1
	s_waitcnt vmcnt(4)
	v_mov_b32_e32 v40, v164
	v_mov_b32_e32 v41, v165
	v_mov_b32_e32 v42, v166
	v_mov_b32_e32 v43, v167
	v_and_b32_e32 v45, 0xffff0000, v40
	v_lshlrev_b32_e32 v44, 16, v40
	v_mul_f32_e32 v45, v45, v45
	v_mfma_f32_32x32x16_bf16 v[20:35], v[64:67], v[40:43], v[20:35]
	v_fmac_f32_e32 v45, v44, v44
	v_add_f32_e32 v1, v45, v1
	v_and_b32_e32 v45, 0xffff0000, v41
	v_lshlrev_b32_e32 v44, 16, v41
	v_mul_f32_e32 v45, v45, v45
	v_fmac_f32_e32 v45, v44, v44
	v_add_f32_e32 v1, v45, v1
	v_and_b32_e32 v45, 0xffff0000, v42
	v_lshlrev_b32_e32 v44, 16, v42
	v_mul_f32_e32 v45, v45, v45
	v_fmac_f32_e32 v45, v44, v44
	v_add_f32_e32 v1, v45, v1
	v_lshlrev_b32_e32 v44, 16, v43
	v_and_b32_e32 v45, 0xffff0000, v43
	v_mfma_f32_32x32x16_bf16 v[20:35], v[68:71], v[40:43], v[20:35]
	v_mul_f32_e32 v45, v45, v45
	v_fmac_f32_e32 v45, v44, v44
	v_add_f32_e32 v1, v45, v1
	s_waitcnt vmcnt(3)
	v_mov_b32_e32 v40, v168
	v_mov_b32_e32 v41, v169
	v_mov_b32_e32 v42, v170
	v_mov_b32_e32 v43, v171
	v_and_b32_e32 v45, 0xffff0000, v40
	v_lshlrev_b32_e32 v44, 16, v40
	v_mul_f32_e32 v45, v45, v45
	v_mfma_f32_32x32x16_bf16 v[20:35], v[72:75], v[40:43], v[20:35]
	v_fmac_f32_e32 v45, v44, v44
	v_add_f32_e32 v1, v45, v1
	v_and_b32_e32 v45, 0xffff0000, v41
	v_lshlrev_b32_e32 v44, 16, v41
	v_mul_f32_e32 v45, v45, v45
	v_fmac_f32_e32 v45, v44, v44
	v_add_f32_e32 v1, v45, v1
	v_and_b32_e32 v45, 0xffff0000, v42
	v_lshlrev_b32_e32 v44, 16, v42
	v_mul_f32_e32 v45, v45, v45
	v_fmac_f32_e32 v45, v44, v44
	v_add_f32_e32 v1, v45, v1
	v_lshlrev_b32_e32 v44, 16, v43
	v_and_b32_e32 v45, 0xffff0000, v43
	v_mfma_f32_32x32x16_bf16 v[20:35], v[76:79], v[40:43], v[20:35]
	v_mul_f32_e32 v45, v45, v45
	v_fmac_f32_e32 v45, v44, v44
	v_add_f32_e32 v1, v45, v1
	s_waitcnt vmcnt(2)
	v_mov_b32_e32 v40, v172
	v_mov_b32_e32 v41, v173
	v_mov_b32_e32 v42, v174
	v_mov_b32_e32 v43, v175
	v_and_b32_e32 v45, 0xffff0000, v40
	v_lshlrev_b32_e32 v44, 16, v40
	v_mul_f32_e32 v45, v45, v45
	v_mfma_f32_32x32x16_bf16 v[20:35], v[80:83], v[40:43], v[20:35]
	v_fmac_f32_e32 v45, v44, v44
	v_add_f32_e32 v1, v45, v1
	v_and_b32_e32 v45, 0xffff0000, v41
	v_lshlrev_b32_e32 v44, 16, v41
	v_mul_f32_e32 v45, v45, v45
	v_fmac_f32_e32 v45, v44, v44
	v_add_f32_e32 v1, v45, v1
	v_and_b32_e32 v45, 0xffff0000, v42
	v_lshlrev_b32_e32 v44, 16, v42
	v_mul_f32_e32 v45, v45, v45
	v_fmac_f32_e32 v45, v44, v44
	v_add_f32_e32 v1, v45, v1
	v_lshlrev_b32_e32 v44, 16, v43
	v_and_b32_e32 v45, 0xffff0000, v43
	v_mfma_f32_32x32x16_bf16 v[20:35], v[84:87], v[40:43], v[20:35]
	v_mul_f32_e32 v45, v45, v45
	v_fmac_f32_e32 v45, v44, v44
	v_add_f32_e32 v1, v45, v1
	s_waitcnt vmcnt(1)
	v_mov_b32_e32 v40, v176
	v_mov_b32_e32 v41, v177
	v_mov_b32_e32 v42, v178
	v_mov_b32_e32 v43, v179
	v_and_b32_e32 v45, 0xffff0000, v40
	v_lshlrev_b32_e32 v44, 16, v40
	v_mul_f32_e32 v45, v45, v45
	v_mfma_f32_32x32x16_bf16 v[20:35], v[96:99], v[40:43], v[20:35]
	v_fmac_f32_e32 v45, v44, v44
	v_add_f32_e32 v1, v45, v1
	v_and_b32_e32 v45, 0xffff0000, v41
	v_lshlrev_b32_e32 v44, 16, v41
	v_mul_f32_e32 v45, v45, v45
	v_fmac_f32_e32 v45, v44, v44
	v_add_f32_e32 v1, v45, v1
	v_and_b32_e32 v45, 0xffff0000, v42
	v_lshlrev_b32_e32 v44, 16, v42
	v_mul_f32_e32 v45, v45, v45
	v_fmac_f32_e32 v45, v44, v44
	v_add_f32_e32 v1, v45, v1
	v_lshlrev_b32_e32 v44, 16, v43
	v_and_b32_e32 v45, 0xffff0000, v43
	v_mfma_f32_32x32x16_bf16 v[20:35], v[100:103], v[40:43], v[20:35]
	v_mul_f32_e32 v45, v45, v45
	v_fmac_f32_e32 v45, v44, v44
	v_add_f32_e32 v44, v45, v1
	s_waitcnt vmcnt(0)
	v_mov_b32_e32 v40, v180
	v_mov_b32_e32 v41, v181
	v_mov_b32_e32 v42, v182
	v_mov_b32_e32 v43, v183
	v_and_b32_e32 v16, 0xffff0000, v40
	v_mfma_f32_32x32x16_bf16 v[20:35], v[92:95], v[40:43], v[20:35]
	v_lshlrev_b32_e32 v1, 16, v40
	v_mul_f32_e32 v16, v16, v16
	v_fmac_f32_e32 v16, v1, v1
	v_and_b32_e32 v17, 0xffff0000, v41
	v_add_f32_e32 v1, v16, v44
	v_lshlrev_b32_e32 v16, 16, v41
	v_mul_f32_e32 v17, v17, v17
	v_fmac_f32_e32 v17, v16, v16
	v_add_f32_e32 v1, v17, v1
	v_and_b32_e32 v17, 0xffff0000, v42
	v_lshlrev_b32_e32 v16, 16, v42
	v_mul_f32_e32 v17, v17, v17
	v_mfma_f32_32x32x16_bf16 v[20:35], v[88:91], v[40:43], v[20:35]
	v_fmac_f32_e32 v17, v16, v16
	v_add_f32_e32 v1, v17, v1
	v_and_b32_e32 v17, 0xffff0000, v43
	v_lshlrev_b32_e32 v16, 16, v43
	v_mul_f32_e32 v17, v17, v17
	v_fmac_f32_e32 v17, v16, v16
	v_add_f32_e32 v16, v17, v1
	v_mov_b32_e32 v17, v16
	s_nop 1
	v_permlane32_swap_b32_e32 v16, v17
	s_and_saveexec_b64 s[4:5], vcc
	v_add_f32_e32 v1, v16, v17
	ds_write_b32 v2, v1 offset:128
	s_or_b64 exec, exec, s[4:5]
	v_add_u32_e32 v1, 0x1080, v104
	ds_write2_b32 v1, v20, v21 offset1:1
	v_add_u32_e32 v1, 0x1088, v104
	ds_write2_b32 v1, v22, v23 offset1:1
	v_add_u32_e32 v1, 0x10a0, v104
	ds_write2_b32 v1, v24, v25 offset1:1
	v_add_u32_e32 v1, 0x10a8, v104
	ds_write2_b32 v1, v26, v27 offset1:1
	v_add_u32_e32 v1, 0x10c0, v104
	ds_write2_b32 v1, v28, v29 offset1:1
	v_add_u32_e32 v1, 0x10c8, v104
	ds_write2_b32 v1, v30, v31 offset1:1
	v_add_u32_e32 v1, 0x10e0, v104
	ds_write2_b32 v1, v32, v33 offset1:1
	v_add_u32_e32 v1, 0x10e8, v104
	v_readlane_b32 s2, v255, 4
	ds_write2_b32 v1, v34, v35 offset1:1
	v_ashrrev_i32_e32 v1, 3, v19
	s_lshl_b32 s82, s2, 5
	s_mov_b32 s83, s73
	v_lshl_add_u32 v2, v1, 2, 0
	s_lshl_b64 s[2:3], s[82:83], 2
	v_add_u32_e32 v2, 0x10800, v2
	s_waitcnt lgkmcnt(0)
	s_add_u32 s0, s0, s2
	s_barrier
	ds_read2st64_b32 v[16:17], v2 offset1:1
	ds_read2st64_b32 v[20:21], v2 offset0:2 offset1:3
	ds_read2st64_b32 v[22:23], v2 offset0:4 offset1:5
	ds_read2st64_b32 v[28:29], v2 offset0:6 offset1:7
	v_lshlrev_b32_e32 v2, 4, v19
	s_addc_u32 s1, s1, s3
	v_and_b32_e32 v30, 0x70, v2
	global_load_dwordx4 v[24:27], v30, s[0:1]
	s_waitcnt lgkmcnt(3)
	v_add_f32_e32 v2, 0, v16
	v_add_f32_e32 v2, v2, v17
	s_waitcnt lgkmcnt(2)
	v_add_f32_e32 v2, v2, v20
	v_add_f32_e32 v2, v2, v21
	s_waitcnt lgkmcnt(1)
	v_add_f32_e32 v2, v2, v22
	v_add_f32_e32 v2, v2, v23
	s_waitcnt lgkmcnt(0)
	v_add_f32_e32 v2, v2, v28
	v_add_f32_e32 v2, v2, v29
	v_fmamk_f32 v2, v2, 0x3a800000, v220
	v_mul_f32_e32 v16, 0x4f800000, v2
	v_cmp_gt_f32_e32 vcc, s93, v2
	v_mov_b32_e32 v23, 0
	v_cmp_gt_i32_e64 s[8:9], 64, v19
	v_cndmask_b32_e32 v2, v2, v16, vcc
	v_sqrt_f32_e32 v16, v2
	v_mov_b32_e32 v56, 0
	v_mov_b32_e32 v54, 0
	v_add_u32_e32 v17, -1, v16
	v_fma_f32 v20, -v17, v16, v2
	v_cmp_ge_f32_e64 s[0:1], 0, v20
	v_add_u32_e32 v20, 1, v16
	s_nop 0
	v_cndmask_b32_e64 v17, v16, v17, s[0:1]
	v_fma_f32 v16, -v20, v16, v2
	v_cmp_lt_f32_e64 s[0:1], 0, v16
	s_nop 1
	v_cndmask_b32_e64 v16, v17, v20, s[0:1]
	v_mul_f32_e32 v17, 0x37800000, v16
	v_cndmask_b32_e32 v16, v16, v17, vcc
	v_cmp_class_f32_e32 vcc, v2, v221
	s_nop 1
	v_cndmask_b32_e32 v2, v16, v2, vcc
	v_div_scale_f32 v16, s[0:1], v2, v2, 1.0
	v_rcp_f32_e32 v17, v16
	s_movk_i32 s0, 0x84
	v_mul_lo_u32 v1, v1, s0
	s_add_i32 s0, 0, 0x20400
	v_fma_f32 v20, -v16, v17, 1.0
	v_fmac_f32_e32 v17, v20, v17
	v_div_scale_f32 v20, vcc, 1.0, v2, 1.0
	v_mul_f32_e32 v21, v20, v17
	v_fma_f32 v22, -v16, v21, v20
	v_fmac_f32_e32 v21, v22, v17
	v_fma_f32 v16, -v16, v21, v20
	v_add3_u32 v22, s0, v1, v30
	v_add3_u32 v1, 0, v30, v1
	v_div_fmas_f32 v16, v16, v17, v21
	v_add_u32_e32 v20, 0x2100, v1
	v_div_fixup_f32 v2, v16, v2, 1.0
	ds_read2_b32 v[16:17], v1 offset1:1
	ds_read2_b32 v[20:21], v20 offset1:1
	v_add_u32_e32 v28, 0x4200, v1
	ds_read2_b32 v[28:29], v28 offset1:1
	ds_read2_b32 v[30:31], v1 offset0:2 offset1:3
	v_add_u32_e32 v32, 0x6300, v1
	v_add_u32_e32 v33, 0x8400, v1
	v_add_u32_e32 v34, 0xa500, v1
	v_add_u32_e32 v40, 0xc600, v1
	s_waitcnt lgkmcnt(3)
	v_pk_add_f32 v[16:17], v[16:17], 0 op_sel_hi:[1,0]
	v_add_u32_e32 v42, 0xe700, v1
	s_waitcnt lgkmcnt(2)
	v_pk_add_f32 v[16:17], v[16:17], v[20:21]
	ds_read2_b32 v[20:21], v32 offset1:1
	ds_read2_b32 v[32:33], v33 offset1:1
	ds_read2_b32 v[34:35], v34 offset1:1
	ds_read2_b32 v[40:41], v40 offset1:1
	s_waitcnt lgkmcnt(5)
	v_pk_add_f32 v[16:17], v[16:17], v[28:29]
	v_add_u32_e32 v28, 0x2108, v1
	s_waitcnt lgkmcnt(3)
	v_pk_add_f32 v[16:17], v[16:17], v[20:21]
	ds_read2_b32 v[20:21], v42 offset1:1
	s_waitcnt lgkmcnt(3)
	v_pk_add_f32 v[16:17], v[16:17], v[32:33]
	v_add_u32_e32 v32, 0x4208, v1
	s_waitcnt lgkmcnt(2)
	v_pk_add_f32 v[16:17], v[16:17], v[34:35]
	v_add_u32_e32 v34, 0x6308, v1
	s_waitcnt lgkmcnt(1)
	v_pk_add_f32 v[16:17], v[16:17], v[40:41]
	ds_read2_b32 v[28:29], v28 offset1:1
	ds_read2_b32 v[32:33], v32 offset1:1
	ds_read2_b32 v[34:35], v34 offset1:1
	s_waitcnt lgkmcnt(3)
	v_pk_add_f32 v[16:17], v[16:17], v[20:21]
	v_add_u32_e32 v20, 0x8408, v1
	v_add_u32_e32 v40, 0xc608, v1
	s_waitcnt vmcnt(0)
	v_pk_fma_f32 v[16:17], v[2:3], v[16:17], v[24:25] op_sel_hi:[0,1,1]
	ds_write2_b32 v22, v16, v17 offset1:1
	v_pk_add_f32 v[16:17], v[30:31], 0 op_sel_hi:[1,0]
	v_add_u32_e32 v24, 0xa508, v1
	s_waitcnt lgkmcnt(3)
	v_pk_add_f32 v[16:17], v[16:17], v[28:29]
	v_add_u32_e32 v1, 0xe708, v1
	s_waitcnt lgkmcnt(2)
	v_pk_add_f32 v[16:17], v[16:17], v[32:33]
	ds_read2_b32 v[20:21], v20 offset1:1
	ds_read2_b32 v[24:25], v24 offset1:1
	ds_read2_b32 v[28:29], v40 offset1:1
	ds_read2_b32 v[30:31], v1 offset1:1
	s_waitcnt lgkmcnt(5)
	v_pk_add_f32 v[16:17], v[16:17], v[34:35]
	s_waitcnt lgkmcnt(3)
	v_pk_add_f32 v[16:17], v[16:17], v[20:21]
	v_mov_b32_e32 v20, 0
	s_waitcnt lgkmcnt(2)
	v_pk_add_f32 v[16:17], v[16:17], v[24:25]
	v_mov_b32_e32 v25, 0
	s_waitcnt lgkmcnt(1)
	v_pk_add_f32 v[16:17], v[16:17], v[28:29]
	v_mov_b32_e32 v21, 0
	s_waitcnt lgkmcnt(0)
	v_pk_add_f32 v[16:17], v[16:17], v[30:31]
	v_mov_b32_e32 v24, 0
	v_pk_fma_f32 v[16:17], v[2:3], v[16:17], v[26:27] op_sel_hi:[0,1,1]
	ds_write2_b32 v22, v16, v17 offset0:2 offset1:3
	v_mov_b32_e32 v26, 0
	v_mov_b32_e32 v22, 0
	v_mov_b32_e32 v2, 0
	v_mov_b32_e32 v16, 0
	v_mov_b32_e32 v17, 0
	s_waitcnt lgkmcnt(0)
	s_barrier
	s_lshl_b32 s100, s89, 3
	s_add_i32 s100, s88, s100
	s_lshl_b32 s100, s100, 11
	v_readlane_b32 s101, v254, 14
	v_lshlrev_b32_e32 v184, 5, v112
	s_add_u32 s100, s101, s100
	v_readlane_b32 s101, v254, 19
	v_mov_b32_e32 v185, 0
	s_addc_u32 s101, s101, 0
	v_lshl_add_u64 v[184:185], s[100:101], 0, v[184:185]
	s_mov_b64 s[100:101], 0x1000
	global_load_dwordx4 v[120:123], v[184:185], off offset:-2032
	global_load_dwordx4 v[124:127], v[184:185], off offset:-2048
	global_load_dwordx4 v[128:131], v[184:185], off offset:16
	global_load_dwordx4 v[132:135], v[184:185], off
	v_lshl_add_u64 v[184:185], v[184:185], 0, s[100:101]
	global_load_dwordx4 v[136:139], v[184:185], off offset:-2032
	global_load_dwordx4 v[140:143], v[184:185], off offset:-2048
	global_load_dwordx4 v[144:147], v[184:185], off offset:16
	global_load_dwordx4 v[148:151], v[184:185], off
	v_lshl_add_u64 v[184:185], v[184:185], 0, s[100:101]
	global_load_dwordx4 v[152:155], v[184:185], off offset:-2032
	global_load_dwordx4 v[156:159], v[184:185], off offset:-2048
	global_load_dwordx4 v[160:163], v[184:185], off offset:16
	global_load_dwordx4 v[164:167], v[184:185], off
	v_lshl_add_u64 v[184:185], v[184:185], 0, s[100:101]
	global_load_dwordx4 v[168:171], v[184:185], off offset:-2032
	global_load_dwordx4 v[172:175], v[184:185], off offset:-2048
	global_load_dwordx4 v[176:179], v[184:185], off offset:16
	global_load_dwordx4 v[180:183], v[184:185], off
	s_and_saveexec_b64 s[84:85], s[8:9]
	s_cbranch_execz .LBB0_1749
	s_movk_i32 s0, 0x84
	v_mul_lo_u32 v1, v19, s0
	v_add_u32_e32 v1, 0, v1
	v_add_u32_e32 v1, 0x20400, v1
	s_mov_b32 s0, 0xff800000
	ds_read2_b32 v[52:53], v1 offset1:1
	ds_read2_b32 v[50:51], v1 offset0:2 offset1:3
	ds_read2_b32 v[48:49], v1 offset0:4 offset1:5
	ds_read2_b32 v[46:47], v1 offset0:6 offset1:7
	ds_read2_b32 v[44:45], v1 offset0:8 offset1:9
	ds_read2_b32 v[42:43], v1 offset0:10 offset1:11
	ds_read2_b32 v[40:41], v1 offset0:12 offset1:13
	ds_read2_b32 v[34:35], v1 offset0:14 offset1:15
	ds_read2_b32 v[32:33], v1 offset0:16 offset1:17
	ds_read2_b32 v[30:31], v1 offset0:18 offset1:19
	ds_read2_b32 v[28:29], v1 offset0:20 offset1:21
	ds_read2_b32 v[26:27], v1 offset0:22 offset1:23
	ds_read2_b32 v[24:25], v1 offset0:24 offset1:25
	ds_read2_b32 v[22:23], v1 offset0:26 offset1:27
	ds_read2_b32 v[20:21], v1 offset0:28 offset1:29
	ds_read2_b32 v[16:17], v1 offset0:30 offset1:31
	s_waitcnt lgkmcnt(14)
	v_cmp_lg_f32_e32 vcc, s0, v52
	v_cmp_nlg_f32_e64 s[0:1], s0, v52
	s_nop 0
	v_cndmask_b32_e32 v1, v18, v52, vcc
	v_cmp_gt_f32_e32 vcc, v53, v1
	s_nop 1
	v_cndmask_b32_e32 v1, v1, v53, vcc
	v_cndmask_b32_e64 v2, 0, 1, vcc
	v_cmp_gt_f32_e32 vcc, v50, v1
	s_nop 1
	v_cndmask_b32_e32 v1, v1, v50, vcc
	v_cndmask_b32_e64 v2, v2, 2, vcc
	v_cmp_gt_f32_e32 vcc, v51, v1
	s_nop 1
	v_cndmask_b32_e32 v1, v1, v51, vcc
	v_cndmask_b32_e64 v2, v2, 3, vcc
	s_waitcnt lgkmcnt(13)
	v_cmp_gt_f32_e32 vcc, v48, v1
	s_nop 1
	v_cndmask_b32_e32 v1, v1, v48, vcc
	v_cndmask_b32_e64 v2, v2, 4, vcc
	v_cmp_gt_f32_e32 vcc, v49, v1
	s_nop 1
	v_cndmask_b32_e32 v1, v1, v49, vcc
	v_cndmask_b32_e64 v2, v2, 5, vcc
	s_waitcnt lgkmcnt(12)
	v_cmp_gt_f32_e32 vcc, v46, v1
	s_nop 1
	v_cndmask_b32_e32 v1, v1, v46, vcc
	v_cndmask_b32_e64 v2, v2, 6, vcc
	v_cmp_gt_f32_e32 vcc, v47, v1
	s_nop 1
	v_cndmask_b32_e32 v1, v1, v47, vcc
	v_cndmask_b32_e64 v2, v2, 7, vcc
	s_waitcnt lgkmcnt(11)
	v_cmp_gt_f32_e32 vcc, v44, v1
	s_nop 1
	v_cndmask_b32_e32 v1, v1, v44, vcc
	v_cndmask_b32_e64 v2, v2, 8, vcc
	v_cmp_gt_f32_e32 vcc, v45, v1
	s_nop 1
	v_cndmask_b32_e32 v1, v1, v45, vcc
	v_cndmask_b32_e64 v2, v2, 9, vcc
	s_waitcnt lgkmcnt(10)
	v_cmp_gt_f32_e32 vcc, v42, v1
	s_nop 1
	v_cndmask_b32_e32 v1, v1, v42, vcc
	v_cndmask_b32_e64 v2, v2, 10, vcc
	v_cmp_gt_f32_e32 vcc, v43, v1
	s_nop 1
	v_cndmask_b32_e32 v1, v1, v43, vcc
	v_cndmask_b32_e64 v2, v2, 11, vcc
	s_waitcnt lgkmcnt(9)
	v_cmp_gt_f32_e32 vcc, v40, v1
	s_nop 1
	v_cndmask_b32_e32 v1, v1, v40, vcc
	v_cndmask_b32_e64 v2, v2, 12, vcc
	v_cmp_gt_f32_e32 vcc, v41, v1
	s_nop 1
	v_cndmask_b32_e32 v1, v1, v41, vcc
	v_cndmask_b32_e64 v2, v2, 13, vcc
	s_waitcnt lgkmcnt(8)
	v_cmp_gt_f32_e32 vcc, v34, v1
	s_nop 1
	v_cndmask_b32_e32 v1, v1, v34, vcc
	v_cndmask_b32_e64 v2, v2, 14, vcc
	v_cmp_gt_f32_e32 vcc, v35, v1
	s_nop 1
	v_cndmask_b32_e32 v1, v1, v35, vcc
	v_cndmask_b32_e64 v2, v2, 15, vcc
	s_waitcnt lgkmcnt(7)
	v_cmp_gt_f32_e32 vcc, v32, v1
	s_nop 1
	v_cndmask_b32_e32 v1, v1, v32, vcc
	v_cndmask_b32_e64 v2, v2, 16, vcc
	v_cmp_gt_f32_e32 vcc, v33, v1
	s_nop 1
	v_cndmask_b32_e32 v1, v1, v33, vcc
	v_cndmask_b32_e64 v2, v2, 17, vcc
	s_waitcnt lgkmcnt(6)
	v_cmp_gt_f32_e32 vcc, v30, v1
	s_nop 1
	v_cndmask_b32_e32 v1, v1, v30, vcc
	v_cndmask_b32_e64 v2, v2, 18, vcc
	v_cmp_gt_f32_e32 vcc, v31, v1
	s_nop 1
	v_cndmask_b32_e32 v1, v1, v31, vcc
	v_cndmask_b32_e64 v2, v2, 19, vcc
	s_waitcnt lgkmcnt(5)
	v_cmp_gt_f32_e32 vcc, v28, v1
	s_nop 1
	v_cndmask_b32_e32 v1, v1, v28, vcc
	v_cndmask_b32_e64 v2, v2, 20, vcc
	v_cmp_gt_f32_e32 vcc, v29, v1
	s_nop 1
	v_cndmask_b32_e32 v1, v1, v29, vcc
	v_cndmask_b32_e64 v2, v2, 21, vcc
	s_waitcnt lgkmcnt(4)
	v_cmp_gt_f32_e32 vcc, v26, v1
	s_nop 1
	v_cndmask_b32_e32 v1, v1, v26, vcc
	v_cndmask_b32_e64 v2, v2, 22, vcc
	v_cmp_gt_f32_e32 vcc, v27, v1
	s_nop 1
	v_cndmask_b32_e32 v1, v1, v27, vcc
	v_cndmask_b32_e64 v2, v2, 23, vcc
	s_waitcnt lgkmcnt(3)
	v_cmp_gt_f32_e32 vcc, v24, v1
	s_nop 1
	v_cndmask_b32_e32 v1, v1, v24, vcc
	v_cndmask_b32_e64 v2, v2, 24, vcc
	v_cmp_gt_f32_e32 vcc, v25, v1
	s_nop 1
	v_cndmask_b32_e32 v1, v1, v25, vcc
	v_cndmask_b32_e64 v2, v2, 25, vcc
	s_waitcnt lgkmcnt(2)
	v_cmp_gt_f32_e32 vcc, v22, v1
	s_nop 1
	v_cndmask_b32_e32 v1, v1, v22, vcc
	v_cndmask_b32_e64 v2, v2, 26, vcc
	v_cmp_gt_f32_e32 vcc, v23, v1
	s_nop 1
	v_cndmask_b32_e32 v1, v1, v23, vcc
	v_cndmask_b32_e64 v2, v2, 27, vcc
	s_waitcnt lgkmcnt(1)
	v_cmp_gt_f32_e32 vcc, v20, v1
	s_nop 1
	v_cndmask_b32_e32 v1, v1, v20, vcc
	v_cndmask_b32_e64 v2, v2, 28, vcc
	v_cmp_gt_f32_e32 vcc, v21, v1
	s_nop 1
	v_cndmask_b32_e32 v1, v1, v21, vcc
	v_cndmask_b32_e64 v2, v2, 29, vcc
	s_waitcnt lgkmcnt(0)
	v_cmp_gt_f32_e32 vcc, v16, v1
	s_nop 1
	v_cndmask_b32_e32 v1, v1, v16, vcc
	v_cndmask_b32_e64 v2, v2, 30, vcc
	v_cmp_gt_f32_e32 vcc, v17, v1
	s_nop 1
	v_cndmask_b32_e64 v2, v2, 31, vcc
	v_cndmask_b32_e32 v55, v1, v17, vcc
	v_cmp_eq_u32_e32 vcc, 0, v2
	s_or_b64 s[0:1], vcc, s[0:1]
	v_cndmask_b32_e64 v1, v52, v18, s[0:1]
	v_cmp_ne_u32_e64 s[66:67], 1, v2
	v_cmp_gt_f32_e32 vcc, v53, v1
	s_and_b64 vcc, s[66:67], vcc
	v_cmp_ne_u32_e64 s[64:65], 2, v2
	v_cndmask_b32_e32 v1, v1, v53, vcc
	v_cndmask_b32_e64 v54, 0, 1, vcc
	v_cmp_gt_f32_e32 vcc, v50, v1
	s_and_b64 vcc, s[64:65], vcc
	v_cmp_ne_u32_e64 s[62:63], 3, v2
	v_cndmask_b32_e32 v1, v1, v50, vcc
	v_cndmask_b32_e64 v54, v54, 2, vcc
	v_cmp_gt_f32_e32 vcc, v51, v1
	s_and_b64 vcc, s[62:63], vcc
	v_cmp_ne_u32_e64 s[60:61], 4, v2
	v_cndmask_b32_e32 v1, v1, v51, vcc
	v_cndmask_b32_e64 v54, v54, 3, vcc
	v_cmp_gt_f32_e32 vcc, v48, v1
	s_and_b64 vcc, s[60:61], vcc
	v_cmp_ne_u32_e64 s[58:59], 5, v2
	v_cndmask_b32_e32 v1, v1, v48, vcc
	v_cndmask_b32_e64 v54, v54, 4, vcc
	v_cmp_gt_f32_e32 vcc, v49, v1
	s_and_b64 vcc, s[58:59], vcc
	v_cmp_ne_u32_e64 s[56:57], 6, v2
	v_cndmask_b32_e32 v1, v1, v49, vcc
	v_cndmask_b32_e64 v54, v54, 5, vcc
	v_cmp_gt_f32_e32 vcc, v46, v1
	s_and_b64 vcc, s[56:57], vcc
	v_cmp_ne_u32_e64 s[54:55], 7, v2
	v_cndmask_b32_e32 v1, v1, v46, vcc
	v_cndmask_b32_e64 v54, v54, 6, vcc
	v_cmp_gt_f32_e32 vcc, v47, v1
	s_and_b64 vcc, s[54:55], vcc
	v_cmp_ne_u32_e64 s[52:53], 8, v2
	v_cndmask_b32_e32 v1, v1, v47, vcc
	v_cndmask_b32_e64 v54, v54, 7, vcc
	v_cmp_gt_f32_e32 vcc, v44, v1
	s_and_b64 vcc, s[52:53], vcc
	v_cmp_ne_u32_e64 s[50:51], 9, v2
	v_cndmask_b32_e32 v1, v1, v44, vcc
	v_cndmask_b32_e64 v54, v54, 8, vcc
	v_cmp_gt_f32_e32 vcc, v45, v1
	s_and_b64 vcc, s[50:51], vcc
	v_cmp_ne_u32_e64 s[48:49], 10, v2
	v_cndmask_b32_e32 v1, v1, v45, vcc
	v_cndmask_b32_e64 v54, v54, 9, vcc
	v_cmp_gt_f32_e32 vcc, v42, v1
	s_and_b64 vcc, s[48:49], vcc
	v_cmp_ne_u32_e64 s[46:47], 11, v2
	v_cndmask_b32_e32 v1, v1, v42, vcc
	v_cndmask_b32_e64 v54, v54, 10, vcc
	v_cmp_gt_f32_e32 vcc, v43, v1
	s_and_b64 vcc, s[46:47], vcc
	v_cmp_ne_u32_e64 s[44:45], 12, v2
	v_cndmask_b32_e32 v1, v1, v43, vcc
	v_cndmask_b32_e64 v54, v54, 11, vcc
	v_cmp_gt_f32_e32 vcc, v40, v1
	s_and_b64 vcc, s[44:45], vcc
	v_cmp_ne_u32_e64 s[42:43], 13, v2
	v_cndmask_b32_e32 v1, v1, v40, vcc
	v_cndmask_b32_e64 v54, v54, 12, vcc
	v_cmp_gt_f32_e32 vcc, v41, v1
	s_and_b64 vcc, s[42:43], vcc
	v_cmp_ne_u32_e64 s[40:41], 14, v2
	v_cndmask_b32_e32 v1, v1, v41, vcc
	v_cndmask_b32_e64 v54, v54, 13, vcc
	v_cmp_gt_f32_e32 vcc, v34, v1
	s_and_b64 vcc, s[40:41], vcc
	v_cmp_ne_u32_e64 s[38:39], 15, v2
	v_cndmask_b32_e32 v1, v1, v34, vcc
	v_cndmask_b32_e64 v54, v54, 14, vcc
	v_cmp_gt_f32_e32 vcc, v35, v1
	s_and_b64 vcc, s[38:39], vcc
	v_cmp_ne_u32_e64 s[36:37], 16, v2
	v_cndmask_b32_e32 v1, v1, v35, vcc
	v_cndmask_b32_e64 v54, v54, 15, vcc
	v_cmp_gt_f32_e32 vcc, v32, v1
	s_and_b64 vcc, s[36:37], vcc
	v_cmp_ne_u32_e64 s[34:35], 17, v2
	v_cndmask_b32_e32 v1, v1, v32, vcc
	v_cndmask_b32_e64 v54, v54, 16, vcc
	v_cmp_gt_f32_e32 vcc, v33, v1
	s_and_b64 vcc, s[34:35], vcc
	v_cmp_ne_u32_e64 s[30:31], 18, v2
	v_cndmask_b32_e32 v1, v1, v33, vcc
	v_cndmask_b32_e64 v54, v54, 17, vcc
	v_cmp_gt_f32_e32 vcc, v30, v1
	s_and_b64 vcc, s[30:31], vcc
	v_cmp_ne_u32_e64 s[28:29], 19, v2
	v_cndmask_b32_e32 v1, v1, v30, vcc
	v_cndmask_b32_e64 v54, v54, 18, vcc
	v_cmp_gt_f32_e32 vcc, v31, v1
	s_and_b64 vcc, s[28:29], vcc
	v_cmp_ne_u32_e64 s[26:27], 20, v2
	v_cndmask_b32_e32 v1, v1, v31, vcc
	v_cndmask_b32_e64 v54, v54, 19, vcc
	v_cmp_gt_f32_e32 vcc, v28, v1
	s_and_b64 vcc, s[26:27], vcc
	v_cmp_ne_u32_e64 s[24:25], 21, v2
	v_cndmask_b32_e32 v1, v1, v28, vcc
	v_cndmask_b32_e64 v54, v54, 20, vcc
	v_cmp_gt_f32_e32 vcc, v29, v1
	s_and_b64 vcc, s[24:25], vcc
	v_cmp_ne_u32_e64 s[22:23], 22, v2
	v_cndmask_b32_e32 v1, v1, v29, vcc
	v_cndmask_b32_e64 v54, v54, 21, vcc
	v_cmp_gt_f32_e32 vcc, v26, v1
	s_and_b64 vcc, s[22:23], vcc
	v_cmp_ne_u32_e64 s[20:21], 23, v2
	v_cndmask_b32_e32 v1, v1, v26, vcc
	v_cndmask_b32_e64 v54, v54, 22, vcc
	v_cmp_gt_f32_e32 vcc, v27, v1
	s_and_b64 vcc, s[20:21], vcc
	v_cmp_ne_u32_e64 s[18:19], 24, v2
	v_cndmask_b32_e32 v1, v1, v27, vcc
	v_cndmask_b32_e64 v54, v54, 23, vcc
	v_cmp_gt_f32_e32 vcc, v24, v1
	s_and_b64 vcc, s[18:19], vcc
	v_cmp_ne_u32_e64 s[16:17], 25, v2
	v_cndmask_b32_e32 v1, v1, v24, vcc
	v_cndmask_b32_e64 v54, v54, 24, vcc
	v_cmp_gt_f32_e32 vcc, v25, v1
	s_and_b64 vcc, s[16:17], vcc
	v_cmp_ne_u32_e64 s[14:15], 26, v2
	v_cndmask_b32_e32 v1, v1, v25, vcc
	v_cndmask_b32_e64 v54, v54, 25, vcc
	v_cmp_gt_f32_e32 vcc, v22, v1
	s_and_b64 vcc, s[14:15], vcc
	v_cmp_ne_u32_e64 s[12:13], 27, v2
	v_cndmask_b32_e32 v1, v1, v22, vcc
	v_cndmask_b32_e64 v54, v54, 26, vcc
	v_cmp_gt_f32_e32 vcc, v23, v1
	s_and_b64 vcc, s[12:13], vcc
	v_cmp_ne_u32_e64 s[10:11], 28, v2
	v_cndmask_b32_e32 v1, v1, v23, vcc
	v_cndmask_b32_e64 v54, v54, 27, vcc
	v_cmp_gt_f32_e32 vcc, v20, v1
	s_and_b64 vcc, s[10:11], vcc
	v_cmp_ne_u32_e64 s[4:5], 29, v2
	v_cndmask_b32_e32 v1, v1, v20, vcc
	v_cndmask_b32_e64 v54, v54, 28, vcc
	v_cmp_gt_f32_e32 vcc, v21, v1
	s_and_b64 vcc, s[4:5], vcc
	v_cmp_ne_u32_e64 s[74:75], 30, v2
	v_cndmask_b32_e32 v1, v1, v21, vcc
	v_cndmask_b32_e64 v54, v54, 29, vcc
	v_cmp_gt_f32_e32 vcc, v16, v1
	s_and_b64 vcc, s[74:75], vcc
	s_nop 0
	v_cndmask_b32_e32 v1, v1, v16, vcc
	v_cndmask_b32_e64 v54, v54, 30, vcc
	v_cmp_ne_u32_e32 vcc, 31, v2
	v_cmp_gt_f32_e64 s[70:71], v17, v1
	s_and_b64 s[70:71], vcc, s[70:71]
	s_nop 0
	v_cndmask_b32_e64 v54, v54, 31, s[70:71]
	v_cndmask_b32_e64 v1, v1, v17, s[70:71]
	v_cmp_eq_u32_e64 s[70:71], 0, v54
	s_or_b64 s[0:1], s[0:1], s[70:71]
	v_cndmask_b32_e64 v56, v52, v18, s[0:1]
	v_cmp_ne_u32_e64 s[70:71], 1, v54
	s_and_b64 s[70:71], s[66:67], s[70:71]
	v_cmp_gt_f32_e64 s[66:67], v53, v56
	s_and_b64 s[66:67], s[70:71], s[66:67]
	v_sub_f32_e32 v1, v1, v55
	v_cndmask_b32_e64 v56, v56, v53, s[66:67]
	v_cndmask_b32_e64 v57, 0, 1, s[66:67]
	v_cmp_ne_u32_e64 s[66:67], 2, v54
	s_and_b64 s[66:67], s[64:65], s[66:67]
	v_cmp_gt_f32_e64 s[64:65], v50, v56
	s_and_b64 s[64:65], s[66:67], s[64:65]
	v_mul_f32_e32 v1, 0x3fb8aa3b, v1
	v_cndmask_b32_e64 v56, v56, v50, s[64:65]
	v_cndmask_b32_e64 v57, v57, 2, s[64:65]
	v_cmp_ne_u32_e64 s[64:65], 3, v54
	s_and_b64 s[64:65], s[62:63], s[64:65]
	v_cmp_gt_f32_e64 s[62:63], v51, v56
	s_and_b64 s[62:63], s[64:65], s[62:63]
	s_nop 0
	v_cndmask_b32_e64 v56, v56, v51, s[62:63]
	v_cndmask_b32_e64 v57, v57, 3, s[62:63]
	v_cmp_ne_u32_e64 s[62:63], 4, v54
	s_and_b64 s[62:63], s[60:61], s[62:63]
	v_cmp_gt_f32_e64 s[60:61], v48, v56
	s_and_b64 s[60:61], s[62:63], s[60:61]
	s_nop 0
	v_cndmask_b32_e64 v56, v56, v48, s[60:61]
	v_cndmask_b32_e64 v57, v57, 4, s[60:61]
	v_cmp_ne_u32_e64 s[60:61], 5, v54
	s_and_b64 s[60:61], s[58:59], s[60:61]
	v_cmp_gt_f32_e64 s[58:59], v49, v56
	s_and_b64 s[58:59], s[60:61], s[58:59]
	s_nop 0
	v_cndmask_b32_e64 v56, v56, v49, s[58:59]
	v_cndmask_b32_e64 v57, v57, 5, s[58:59]
	v_cmp_ne_u32_e64 s[58:59], 6, v54
	s_and_b64 s[58:59], s[56:57], s[58:59]
	v_cmp_gt_f32_e64 s[56:57], v46, v56
	s_and_b64 s[56:57], s[58:59], s[56:57]
	s_nop 0
	v_cndmask_b32_e64 v56, v56, v46, s[56:57]
	v_cndmask_b32_e64 v57, v57, 6, s[56:57]
	v_cmp_ne_u32_e64 s[56:57], 7, v54
	s_and_b64 s[56:57], s[54:55], s[56:57]
	v_cmp_gt_f32_e64 s[54:55], v47, v56
	s_and_b64 s[54:55], s[56:57], s[54:55]
	s_nop 0
	v_cndmask_b32_e64 v56, v56, v47, s[54:55]
	v_cndmask_b32_e64 v57, v57, 7, s[54:55]
	v_cmp_ne_u32_e64 s[54:55], 8, v54
	s_and_b64 s[54:55], s[52:53], s[54:55]
	v_cmp_gt_f32_e64 s[52:53], v44, v56
	s_and_b64 s[52:53], s[54:55], s[52:53]
	s_nop 0
	v_cndmask_b32_e64 v56, v56, v44, s[52:53]
	v_cndmask_b32_e64 v57, v57, 8, s[52:53]
	v_cmp_ne_u32_e64 s[52:53], 9, v54
	s_and_b64 s[52:53], s[50:51], s[52:53]
	v_cmp_gt_f32_e64 s[50:51], v45, v56
	s_and_b64 s[50:51], s[52:53], s[50:51]
	s_nop 0
	v_cndmask_b32_e64 v56, v56, v45, s[50:51]
	v_cndmask_b32_e64 v57, v57, 9, s[50:51]
	v_cmp_ne_u32_e64 s[50:51], 10, v54
	s_and_b64 s[50:51], s[48:49], s[50:51]
	v_cmp_gt_f32_e64 s[48:49], v42, v56
	s_and_b64 s[48:49], s[50:51], s[48:49]
	s_nop 0
	v_cndmask_b32_e64 v56, v56, v42, s[48:49]
	v_cndmask_b32_e64 v57, v57, 10, s[48:49]
	v_cmp_ne_u32_e64 s[48:49], 11, v54
	s_and_b64 s[48:49], s[46:47], s[48:49]
	v_cmp_gt_f32_e64 s[46:47], v43, v56
	s_and_b64 s[46:47], s[48:49], s[46:47]
	s_nop 0
	v_cndmask_b32_e64 v56, v56, v43, s[46:47]
	v_cndmask_b32_e64 v57, v57, 11, s[46:47]
	v_cmp_ne_u32_e64 s[46:47], 12, v54
	s_and_b64 s[46:47], s[44:45], s[46:47]
	v_cmp_gt_f32_e64 s[44:45], v40, v56
	s_and_b64 s[44:45], s[46:47], s[44:45]
	s_nop 0
	v_cndmask_b32_e64 v56, v56, v40, s[44:45]
	v_cndmask_b32_e64 v57, v57, 12, s[44:45]
	v_cmp_ne_u32_e64 s[44:45], 13, v54
	s_and_b64 s[44:45], s[42:43], s[44:45]
	v_cmp_gt_f32_e64 s[42:43], v41, v56
	s_and_b64 s[42:43], s[44:45], s[42:43]
	s_nop 0
	v_cndmask_b32_e64 v56, v56, v41, s[42:43]
	v_cndmask_b32_e64 v57, v57, 13, s[42:43]
	v_cmp_ne_u32_e64 s[42:43], 14, v54
	s_and_b64 s[42:43], s[40:41], s[42:43]
	v_cmp_gt_f32_e64 s[40:41], v34, v56
	s_and_b64 s[40:41], s[42:43], s[40:41]
	s_nop 0
	v_cndmask_b32_e64 v56, v56, v34, s[40:41]
	v_cndmask_b32_e64 v57, v57, 14, s[40:41]
	v_cmp_ne_u32_e64 s[40:41], 15, v54
	s_and_b64 s[40:41], s[38:39], s[40:41]
	v_cmp_gt_f32_e64 s[38:39], v35, v56
	s_and_b64 s[38:39], s[40:41], s[38:39]
	s_nop 0
	v_cndmask_b32_e64 v56, v56, v35, s[38:39]
	v_cndmask_b32_e64 v57, v57, 15, s[38:39]
	v_cmp_ne_u32_e64 s[38:39], 16, v54
	s_and_b64 s[38:39], s[36:37], s[38:39]
	v_cmp_gt_f32_e64 s[36:37], v32, v56
	s_and_b64 s[36:37], s[38:39], s[36:37]
	s_nop 0
	v_cndmask_b32_e64 v56, v56, v32, s[36:37]
	v_cndmask_b32_e64 v57, v57, 16, s[36:37]
	v_cmp_ne_u32_e64 s[36:37], 17, v54
	s_and_b64 s[36:37], s[34:35], s[36:37]
	v_cmp_gt_f32_e64 s[34:35], v33, v56
	s_and_b64 s[34:35], s[36:37], s[34:35]
	s_nop 0
	v_cndmask_b32_e64 v56, v56, v33, s[34:35]
	v_cndmask_b32_e64 v57, v57, 17, s[34:35]
	v_cmp_ne_u32_e64 s[34:35], 18, v54
	s_and_b64 s[34:35], s[30:31], s[34:35]
	v_cmp_gt_f32_e64 s[30:31], v30, v56
	s_and_b64 s[30:31], s[34:35], s[30:31]
	s_nop 0
	v_cndmask_b32_e64 v56, v56, v30, s[30:31]
	v_cndmask_b32_e64 v57, v57, 18, s[30:31]
	v_cmp_ne_u32_e64 s[30:31], 19, v54
	s_and_b64 s[30:31], s[28:29], s[30:31]
	v_cmp_gt_f32_e64 s[28:29], v31, v56
	s_and_b64 s[28:29], s[30:31], s[28:29]
	s_nop 0
	v_cndmask_b32_e64 v56, v56, v31, s[28:29]
	v_cndmask_b32_e64 v57, v57, 19, s[28:29]
	v_cmp_ne_u32_e64 s[28:29], 20, v54
	s_and_b64 s[28:29], s[26:27], s[28:29]
	v_cmp_gt_f32_e64 s[26:27], v28, v56
	s_and_b64 s[26:27], s[28:29], s[26:27]
	s_nop 0
	v_cndmask_b32_e64 v56, v56, v28, s[26:27]
	v_cndmask_b32_e64 v57, v57, 20, s[26:27]
	v_cmp_ne_u32_e64 s[26:27], 21, v54
	s_and_b64 s[26:27], s[24:25], s[26:27]
	v_cmp_gt_f32_e64 s[24:25], v29, v56
	s_and_b64 s[24:25], s[26:27], s[24:25]
	s_nop 0
	v_cndmask_b32_e64 v56, v56, v29, s[24:25]
	v_cndmask_b32_e64 v57, v57, 21, s[24:25]
	v_cmp_ne_u32_e64 s[24:25], 22, v54
	s_and_b64 s[24:25], s[22:23], s[24:25]
	v_cmp_gt_f32_e64 s[22:23], v26, v56
	s_and_b64 s[22:23], s[24:25], s[22:23]
	s_nop 0
	v_cndmask_b32_e64 v56, v56, v26, s[22:23]
	v_cndmask_b32_e64 v57, v57, 22, s[22:23]
	v_cmp_ne_u32_e64 s[22:23], 23, v54
	s_and_b64 s[22:23], s[20:21], s[22:23]
	v_cmp_gt_f32_e64 s[20:21], v27, v56
	s_and_b64 s[20:21], s[22:23], s[20:21]
	s_nop 0
	v_cndmask_b32_e64 v56, v56, v27, s[20:21]
	v_cndmask_b32_e64 v57, v57, 23, s[20:21]
	v_cmp_ne_u32_e64 s[20:21], 24, v54
	s_and_b64 s[20:21], s[18:19], s[20:21]
	v_cmp_gt_f32_e64 s[18:19], v24, v56
	s_and_b64 s[18:19], s[20:21], s[18:19]
	s_nop 0
	v_cndmask_b32_e64 v56, v56, v24, s[18:19]
	v_cndmask_b32_e64 v57, v57, 24, s[18:19]
	v_cmp_ne_u32_e64 s[18:19], 25, v54
	s_and_b64 s[18:19], s[16:17], s[18:19]
	v_cmp_gt_f32_e64 s[16:17], v25, v56
	s_and_b64 s[16:17], s[18:19], s[16:17]
	s_nop 0
	v_cndmask_b32_e64 v56, v56, v25, s[16:17]
	v_cndmask_b32_e64 v57, v57, 25, s[16:17]
	v_cmp_ne_u32_e64 s[16:17], 26, v54
	s_and_b64 s[16:17], s[14:15], s[16:17]
	v_cmp_gt_f32_e64 s[14:15], v22, v56
	s_and_b64 s[14:15], s[16:17], s[14:15]
	s_nop 0
	v_cndmask_b32_e64 v56, v56, v22, s[14:15]
	v_cndmask_b32_e64 v57, v57, 26, s[14:15]
	v_cmp_ne_u32_e64 s[14:15], 27, v54
	s_and_b64 s[14:15], s[12:13], s[14:15]
	v_cmp_gt_f32_e64 s[12:13], v23, v56
	s_and_b64 s[12:13], s[14:15], s[12:13]
	s_nop 0
	v_cndmask_b32_e64 v56, v56, v23, s[12:13]
	v_cndmask_b32_e64 v57, v57, 27, s[12:13]
	v_cmp_ne_u32_e64 s[12:13], 28, v54
	s_and_b64 s[12:13], s[10:11], s[12:13]
	v_cmp_gt_f32_e64 s[10:11], v20, v56
	s_and_b64 s[10:11], s[12:13], s[10:11]
	s_nop 0
	v_cndmask_b32_e64 v56, v56, v20, s[10:11]
	v_cndmask_b32_e64 v57, v57, 28, s[10:11]
	v_cmp_ne_u32_e64 s[10:11], 29, v54
	s_and_b64 s[10:11], s[4:5], s[10:11]
	v_cmp_gt_f32_e64 s[4:5], v21, v56
	s_and_b64 s[4:5], s[10:11], s[4:5]
	s_nop 0
	v_cndmask_b32_e64 v56, v56, v21, s[4:5]
	v_cndmask_b32_e64 v57, v57, 29, s[4:5]
	v_cmp_ne_u32_e64 s[4:5], 30, v54
	s_and_b64 s[74:75], s[74:75], s[4:5]
	v_cmp_gt_f32_e64 s[4:5], v16, v56
	s_and_b64 s[4:5], s[74:75], s[4:5]
	s_nop 0
	v_cndmask_b32_e64 v56, v56, v16, s[4:5]
	v_cndmask_b32_e64 v57, v57, 30, s[4:5]
	v_cmp_ne_u32_e64 s[4:5], 31, v54
	s_and_b64 s[86:87], vcc, s[4:5]
	v_cmp_gt_f32_e32 vcc, v17, v56
	s_and_b64 vcc, s[86:87], vcc
	s_nop 0
	v_cndmask_b32_e32 v58, v56, v17, vcc
	v_cndmask_b32_e64 v56, v57, 31, vcc
	v_cmp_eq_u32_e32 vcc, 0, v56
	s_or_b64 vcc, s[0:1], vcc
	v_cmp_ne_u32_e64 s[4:5], 30, v56
	v_cndmask_b32_e32 v52, v52, v18, vcc
	v_cmp_ne_u32_e32 vcc, 1, v56
	s_and_b64 s[0:1], s[70:71], vcc
	v_cmp_gt_f32_e32 vcc, v53, v52
	s_and_b64 vcc, s[0:1], vcc
	s_nop 0
	v_cndmask_b32_e32 v52, v52, v53, vcc
	v_cndmask_b32_e64 v53, 0, 1, vcc
	v_cmp_ne_u32_e32 vcc, 2, v56
	s_and_b64 s[0:1], s[66:67], vcc
	v_cmp_gt_f32_e32 vcc, v50, v52
	s_and_b64 vcc, s[0:1], vcc
	s_nop 0
	v_cndmask_b32_e32 v50, v52, v50, vcc
	v_cndmask_b32_e64 v52, v53, 2, vcc
	v_cmp_ne_u32_e32 vcc, 3, v56
	s_and_b64 s[0:1], s[64:65], vcc
	v_cmp_gt_f32_e32 vcc, v51, v50
	s_and_b64 vcc, s[0:1], vcc
	s_nop 0
	v_cndmask_b32_e32 v50, v50, v51, vcc
	v_cndmask_b32_e64 v51, v52, 3, vcc
	v_cmp_ne_u32_e32 vcc, 4, v56
	s_and_b64 s[0:1], s[62:63], vcc
	v_cmp_gt_f32_e32 vcc, v48, v50
	s_and_b64 vcc, s[0:1], vcc
	s_nop 0
	v_cndmask_b32_e32 v48, v50, v48, vcc
	v_cndmask_b32_e64 v50, v51, 4, vcc
	v_cmp_ne_u32_e32 vcc, 5, v56
	s_and_b64 s[0:1], s[60:61], vcc
	v_cmp_gt_f32_e32 vcc, v49, v48
	s_and_b64 vcc, s[0:1], vcc
	s_nop 0
	v_cndmask_b32_e32 v48, v48, v49, vcc
	v_cndmask_b32_e64 v49, v50, 5, vcc
	v_cmp_ne_u32_e32 vcc, 6, v56
	s_and_b64 s[0:1], s[58:59], vcc
	v_cmp_gt_f32_e32 vcc, v46, v48
	s_and_b64 vcc, s[0:1], vcc
	s_nop 0
	v_cndmask_b32_e32 v46, v48, v46, vcc
	v_cndmask_b32_e64 v48, v49, 6, vcc
	v_cmp_ne_u32_e32 vcc, 7, v56
	s_and_b64 s[0:1], s[56:57], vcc
	v_cmp_gt_f32_e32 vcc, v47, v46
	s_and_b64 vcc, s[0:1], vcc
	s_nop 0
	v_cndmask_b32_e32 v46, v46, v47, vcc
	v_cndmask_b32_e64 v47, v48, 7, vcc
	v_cmp_ne_u32_e32 vcc, 8, v56
	s_and_b64 s[0:1], s[54:55], vcc
	v_cmp_gt_f32_e32 vcc, v44, v46
	s_and_b64 vcc, s[0:1], vcc
	s_nop 0
	v_cndmask_b32_e32 v44, v46, v44, vcc
	v_cndmask_b32_e64 v46, v47, 8, vcc
	v_cmp_ne_u32_e32 vcc, 9, v56
	s_and_b64 s[0:1], s[52:53], vcc
	v_cmp_gt_f32_e32 vcc, v45, v44
	s_and_b64 vcc, s[0:1], vcc
	s_nop 0
	v_cndmask_b32_e32 v44, v44, v45, vcc
	v_cndmask_b32_e64 v45, v46, 9, vcc
	v_cmp_ne_u32_e32 vcc, 10, v56
	s_and_b64 s[0:1], s[50:51], vcc
	v_cmp_gt_f32_e32 vcc, v42, v44
	s_and_b64 vcc, s[0:1], vcc
	s_nop 0
	v_cndmask_b32_e32 v42, v44, v42, vcc
	v_cndmask_b32_e64 v44, v45, 10, vcc
	v_cmp_ne_u32_e32 vcc, 11, v56
	s_and_b64 s[0:1], s[48:49], vcc
	v_cmp_gt_f32_e32 vcc, v43, v42
	s_and_b64 vcc, s[0:1], vcc
	s_nop 0
	v_cndmask_b32_e32 v42, v42, v43, vcc
	v_cndmask_b32_e64 v43, v44, 11, vcc
	v_cmp_ne_u32_e32 vcc, 12, v56
	s_and_b64 s[0:1], s[46:47], vcc
	v_cmp_gt_f32_e32 vcc, v40, v42
	s_and_b64 vcc, s[0:1], vcc
	s_nop 0
	v_cndmask_b32_e32 v40, v42, v40, vcc
	v_cndmask_b32_e64 v42, v43, 12, vcc
	v_cmp_ne_u32_e32 vcc, 13, v56
	s_and_b64 s[0:1], s[44:45], vcc
	v_cmp_gt_f32_e32 vcc, v41, v40
	s_and_b64 vcc, s[0:1], vcc
	s_nop 0
	v_cndmask_b32_e32 v40, v40, v41, vcc
	v_cndmask_b32_e64 v41, v42, 13, vcc
	v_cmp_ne_u32_e32 vcc, 14, v56
	s_and_b64 s[0:1], s[42:43], vcc
	v_cmp_gt_f32_e32 vcc, v34, v40
	s_and_b64 vcc, s[0:1], vcc
	s_nop 0
	v_cndmask_b32_e32 v34, v40, v34, vcc
	v_cndmask_b32_e64 v40, v41, 14, vcc
	v_cmp_ne_u32_e32 vcc, 15, v56
	s_and_b64 s[0:1], s[40:41], vcc
	v_cmp_gt_f32_e32 vcc, v35, v34
	s_and_b64 vcc, s[0:1], vcc
	s_nop 0
	v_cndmask_b32_e32 v34, v34, v35, vcc
	v_cndmask_b32_e64 v35, v40, 15, vcc
	v_cmp_ne_u32_e32 vcc, 16, v56
	s_and_b64 s[0:1], s[38:39], vcc
	v_cmp_gt_f32_e32 vcc, v32, v34
	s_and_b64 vcc, s[0:1], vcc
	s_nop 0
	v_cndmask_b32_e32 v32, v34, v32, vcc
	v_cndmask_b32_e64 v34, v35, 16, vcc
	v_cmp_ne_u32_e32 vcc, 17, v56
	s_and_b64 s[0:1], s[36:37], vcc
	v_cmp_gt_f32_e32 vcc, v33, v32
	s_and_b64 vcc, s[0:1], vcc
	s_nop 0
	v_cndmask_b32_e32 v32, v32, v33, vcc
	v_cndmask_b32_e64 v33, v34, 17, vcc
	v_cmp_ne_u32_e32 vcc, 18, v56
	s_and_b64 s[0:1], s[34:35], vcc
	v_cmp_gt_f32_e32 vcc, v30, v32
	s_and_b64 vcc, s[0:1], vcc
	s_nop 0
	v_cndmask_b32_e32 v30, v32, v30, vcc
	v_cndmask_b32_e64 v32, v33, 18, vcc
	v_cmp_ne_u32_e32 vcc, 19, v56
	s_and_b64 s[0:1], s[30:31], vcc
	v_cmp_gt_f32_e32 vcc, v31, v30
	s_and_b64 vcc, s[0:1], vcc
	s_nop 0
	v_cndmask_b32_e32 v30, v30, v31, vcc
	v_cndmask_b32_e64 v31, v32, 19, vcc
	v_cmp_ne_u32_e32 vcc, 20, v56
	s_and_b64 s[0:1], s[28:29], vcc
	v_cmp_gt_f32_e32 vcc, v28, v30
	s_and_b64 vcc, s[0:1], vcc
	s_nop 0
	v_cndmask_b32_e32 v28, v30, v28, vcc
	v_cndmask_b32_e64 v30, v31, 20, vcc
	v_cmp_ne_u32_e32 vcc, 21, v56
	s_and_b64 s[0:1], s[26:27], vcc
	v_cmp_gt_f32_e32 vcc, v29, v28
	s_and_b64 vcc, s[0:1], vcc
	s_nop 0
	v_cndmask_b32_e32 v28, v28, v29, vcc
	v_cndmask_b32_e64 v29, v30, 21, vcc
	v_cmp_ne_u32_e32 vcc, 22, v56
	s_and_b64 s[0:1], s[24:25], vcc
	v_cmp_gt_f32_e32 vcc, v26, v28
	s_and_b64 vcc, s[0:1], vcc
	s_nop 0
	v_cndmask_b32_e32 v26, v28, v26, vcc
	v_cndmask_b32_e64 v28, v29, 22, vcc
	v_cmp_ne_u32_e32 vcc, 23, v56
	s_and_b64 s[0:1], s[22:23], vcc
	v_cmp_gt_f32_e32 vcc, v27, v26
	s_and_b64 vcc, s[0:1], vcc
	s_nop 0
	v_cndmask_b32_e32 v26, v26, v27, vcc
	v_cndmask_b32_e64 v27, v28, 23, vcc
	v_cmp_ne_u32_e32 vcc, 24, v56
	s_and_b64 s[0:1], s[20:21], vcc
	v_cmp_gt_f32_e32 vcc, v24, v26
	s_and_b64 vcc, s[0:1], vcc
	s_nop 0
	v_cndmask_b32_e32 v24, v26, v24, vcc
	v_cndmask_b32_e64 v26, v27, 24, vcc
	v_cmp_ne_u32_e32 vcc, 25, v56
	s_and_b64 s[0:1], s[18:19], vcc
	v_cmp_gt_f32_e32 vcc, v25, v24
	s_and_b64 vcc, s[0:1], vcc
	s_nop 0
	v_cndmask_b32_e32 v24, v24, v25, vcc
	v_cndmask_b32_e64 v25, v26, 25, vcc
	v_cmp_ne_u32_e32 vcc, 26, v56
	s_and_b64 s[0:1], s[16:17], vcc
	v_cmp_gt_f32_e32 vcc, v22, v24
	s_and_b64 vcc, s[0:1], vcc
	s_nop 0
	v_cndmask_b32_e32 v22, v24, v22, vcc
	v_cndmask_b32_e64 v24, v25, 26, vcc
	v_cmp_ne_u32_e32 vcc, 27, v56
	s_and_b64 s[0:1], s[14:15], vcc
	v_cmp_gt_f32_e32 vcc, v23, v22
	s_and_b64 vcc, s[0:1], vcc
	s_nop 0
	v_cndmask_b32_e32 v22, v22, v23, vcc
	v_cndmask_b32_e64 v23, v24, 27, vcc
	v_cmp_ne_u32_e32 vcc, 28, v56
	s_and_b64 s[0:1], s[12:13], vcc
	v_cmp_gt_f32_e32 vcc, v20, v22
	s_and_b64 vcc, s[0:1], vcc
	v_cmp_ne_u32_e64 s[0:1], 29, v56
	v_cndmask_b32_e32 v20, v22, v20, vcc
	s_and_b64 s[2:3], s[10:11], s[0:1]
	v_cmp_gt_f32_e64 s[0:1], v21, v20
	s_and_b64 s[0:1], s[2:3], s[0:1]
	s_and_b64 s[2:3], s[74:75], s[4:5]
	v_cndmask_b32_e64 v20, v20, v21, s[0:1]
	v_cmp_gt_f32_e64 s[4:5], v16, v20
	s_and_b64 s[4:5], s[2:3], s[4:5]
	v_cmp_ne_u32_e64 s[10:11], 31, v56
	v_cndmask_b32_e64 v16, v20, v16, s[4:5]
	s_and_b64 s[2:3], s[86:87], s[10:11]
	v_cmp_gt_f32_e64 s[10:11], v17, v16
	s_and_b64 s[10:11], s[2:3], s[10:11]
	s_mov_b32 s74, 0x3c800000
	v_cndmask_b32_e64 v20, v16, v17, s[10:11]
	v_exp_f32_e32 v16, v1
	v_sub_f32_e32 v1, v58, v55
	v_mul_f32_e32 v1, 0x3fb8aa3b, v1
	v_exp_f32_e32 v17, v1
	v_sub_f32_e32 v1, v20, v55
	v_mul_f32_e32 v1, 0x3fb8aa3b, v1
	v_exp_f32_e32 v1, v1
	v_add_f32_e32 v21, 1.0, v16
	v_add_f32_e32 v21, v21, v17
	v_cndmask_b32_e64 v20, v23, 28, vcc
	v_add_f32_e32 v23, v21, v1
	v_div_scale_f32 v21, s[2:3], v23, v23, 1.0
	v_rcp_f32_e32 v27, v21
	v_cndmask_b32_e64 v20, v20, 29, s[0:1]
	v_cndmask_b32_e64 v20, v20, 30, s[4:5]
	v_cndmask_b32_e64 v24, v20, 31, s[10:11]
	v_fma_f32 v20, -v21, v27, 1.0
	v_fmac_f32_e32 v27, v20, v27
	v_div_scale_f32 v20, vcc, 1.0, v23, 1.0
	v_mul_f32_e32 v28, v20, v27
	v_fma_f32 v22, -v21, v28, v20
	v_fmac_f32_e32 v28, v22, v27
	s_add_i32 s0, 0, 0x22500
	v_fma_f32 v20, -v21, v28, v20
	v_lshl_add_u32 v21, v2, 2, s0
	ds_add_rtn_u32 v21, v21, v219
	v_lshl_add_u32 v22, v54, 2, s0
	ds_add_rtn_u32 v22, v22, v219
	v_lshl_add_u32 v25, v56, 2, s0
	ds_add_rtn_u32 v26, v25, v219
	v_lshl_add_u32 v25, v24, 2, s0
	ds_add_rtn_u32 v25, v25, v219
	v_div_fmas_f32 v20, v20, v27, v28
	v_div_fixup_f32 v20, v20, v23, 1.0
	s_mov_b64 s[86:87], 0x80
	s_waitcnt lgkmcnt(3)
	v_pk_mul_f32 v[16:17], v[16:17], v[20:21] op_sel_hi:[1,0]
	v_mul_f32_e32 v23, v1, v20

.LBB0_1753:
	s_or_b64 exec, exec, s[0:1]
	v_lshlrev_b32_e32 v27, 2, v112
	s_waitcnt lgkmcnt(0)
	s_barrier
	s_waitcnt vmcnt(0)
	s_and_saveexec_b64 s[0:1], s[8:9]
	s_cbranch_execz .LBB0_1755
	s_add_i32 s2, 0, 0x22580
	v_lshl_add_u32 v1, v2, 2, s2
	ds_read_b32 v1, v1
	v_lshl_add_u32 v28, v19, 4, 0
	v_add_u32_e32 v34, 0x22600, v28
	v_lshl_add_u32 v29, v54, 2, s2
	v_add_u32_e32 v30, s88, v19
	s_waitcnt lgkmcnt(0)
	v_add_u32_e32 v1, v1, v21
	v_lshl_or_b32 v28, v2, 16, v1
	ds_write_b32 v34, v28
	ds_read_b32 v1, v29
	v_lshl_add_u32 v2, v56, 2, s2
	v_ashrrev_i32_e32 v31, 31, v30
	v_mov_b32_e32 v21, v16
	s_waitcnt lgkmcnt(0)
	v_add_u32_e32 v1, v1, v22
	v_lshl_or_b32 v29, v54, 16, v1
	ds_write_b32 v34, v29 offset:4
	ds_read_b32 v1, v2
	v_mov_b32_e32 v22, v17
	v_lshl_add_u64 v[16:17], v[30:31], 4, s[80:81]
	v_lshl_add_u32 v2, v24, 2, s2
	v_add_co_u32_e32 v32, vcc, 0x1f00000, v16
	s_waitcnt lgkmcnt(0)
	v_add_u32_e32 v1, v1, v26
	v_lshl_or_b32 v30, v56, 16, v1
	ds_write_b32 v34, v30 offset:8
	ds_read_b32 v1, v2
	v_addc_co_u32_e32 v33, vcc, 0, v17, vcc
	v_add_co_u32_e32 v16, vcc, 0x1f80000, v16
	s_waitcnt lgkmcnt(0)
	v_add_u32_e32 v1, v1, v25
	v_lshl_or_b32 v31, v24, 16, v1
	v_addc_co_u32_e32 v17, vcc, 0, v17, vcc
	ds_write_b32 v34, v31 offset:12
	global_store_dwordx4 v[32:33], v[28:31], off
	global_store_dwordx4 v[16:17], v[20:23], off

.LBB0_1756:
	s_or_b64 exec, exec, s[0:1]
	v_mov_b64_e32 v[120:121], v[136:137]
	v_mov_b64_e32 v[122:123], v[138:139]
	v_mov_b64_e32 v[124:125], v[140:141]
	v_mov_b64_e32 v[126:127], v[142:143]
	v_mov_b64_e32 v[128:129], v[144:145]
	v_mov_b64_e32 v[130:131], v[146:147]
	v_mov_b64_e32 v[132:133], v[148:149]
	v_mov_b64_e32 v[134:135], v[150:151]
	v_mov_b64_e32 v[136:137], v[152:153]
	v_mov_b64_e32 v[138:139], v[154:155]
	v_mov_b64_e32 v[140:141], v[156:157]
	v_mov_b64_e32 v[142:143], v[158:159]
	v_mov_b64_e32 v[144:145], v[160:161]
	v_mov_b64_e32 v[146:147], v[162:163]
	v_mov_b64_e32 v[148:149], v[164:165]
	v_mov_b64_e32 v[150:151], v[166:167]
	v_mov_b64_e32 v[152:153], v[168:169]
	v_mov_b64_e32 v[154:155], v[170:171]
	v_mov_b64_e32 v[156:157], v[172:173]
	v_mov_b64_e32 v[158:159], v[174:175]
	v_mov_b64_e32 v[160:161], v[176:177]
	v_mov_b64_e32 v[162:163], v[178:179]
	v_mov_b64_e32 v[164:165], v[180:181]
	v_mov_b64_e32 v[166:167], v[182:183]
	s_mov_b64 s[0:1], 0x800
	s_add_i32 s2, s2, 32
	s_add_i32 s8, s8, 2
	v_lshl_add_u64 v[16:17], v[16:17], 0, s[0:1]
	s_mov_b64 s[0:1], 0x1000
	s_cmp_lg_u32 s2, 0
	v_lshl_add_u64 v[20:21], v[20:21], 0, s[0:1]
	s_cbranch_scc0 .LBB0_1761
.LBB0_1757:
	v_lshl_add_u64 v[24:25], v[20:21], 0, s[72:73]
	v_mov_b64_e32 v[32:33], v[120:121]
	v_mov_b64_e32 v[34:35], v[122:123]
	v_mov_b64_e32 v[40:41], v[124:125]
	v_mov_b64_e32 v[42:43], v[126:127]
	v_lshlrev_b32_e32 v26, 16, v34
	v_lshlrev_b32_e32 v44, 16, v40
	v_and_b32_e32 v45, 0xffff0000, v40
	v_lshlrev_b32_e32 v40, 16, v41
	v_and_b32_e32 v41, 0xffff0000, v41
	v_lshlrev_b32_e32 v47, 16, v43
	v_lshlrev_b32_e32 v46, 16, v42
	v_and_b32_e32 v43, 0xffff0000, v43
	v_and_b32_e32 v42, 0xffff0000, v42
	v_mul_f32_e32 v2, v44, v44
	v_mul_f32_e32 v22, v40, v40
	v_lshlrev_b32_e32 v48, 16, v32
	v_and_b32_e32 v49, 0xffff0000, v32
	v_lshlrev_b32_e32 v50, 16, v33
	v_and_b32_e32 v51, 0xffff0000, v33
	v_pk_mul_f32 v[32:33], v[42:43], v[42:43]
	v_pk_fma_f32 v[56:57], v[44:45], v[44:45], v[2:3] op_sel_hi:[1,1,0]
	v_pk_fma_f32 v[22:23], v[40:41], v[40:41], v[22:23] op_sel_hi:[1,1,0]
	v_and_b32_e32 v31, 0xffff0000, v34
	v_mul_f32_e32 v34, v48, v48
	v_mul_f32_e32 v52, v50, v50
	v_mov_b32_e32 v54, v26
	v_pk_fma_f32 v[32:33], v[46:47], v[46:47], v[32:33]
	v_mov_b32_e32 v27, v57
	v_mov_b32_e32 v55, v23
	v_lshlrev_b32_e32 v28, 16, v35
	v_and_b32_e32 v29, 0xffff0000, v35
	v_pk_fma_f32 v[34:35], v[48:49], v[48:49], v[34:35] op_sel_hi:[1,1,0]
	v_pk_fma_f32 v[52:53], v[50:51], v[50:51], v[52:53] op_sel_hi:[1,1,0]
	v_pk_add_f32 v[32:33], v[32:33], v[32:33] op_sel_hi:[0,1]
	v_pk_add_f32 v[22:23], v[56:57], v[22:23]
	v_pk_mul_f32 v[54:55], v[26:27], v[54:55]
	v_mul_f32_e32 v34, v28, v28
	v_mul_f32_e32 v52, v29, v29
	v_mul_f32_e32 v32, v31, v31
	v_mov_b32_e32 v55, v23
	v_pk_add_f32 v[34:35], v[34:35], v[52:53]
	v_pk_add_f32 v[22:23], v[54:55], v[32:33]
	v_mov_b32_e32 v52, v46
	v_pk_add_f32 v[22:23], v[22:23], v[34:35]
	v_mov_b32_e32 v53, v42
	v_add_f32_e32 v2, v22, v23
	v_mov_b32_e32 v42, v47
	v_mov_b32_e32 v32, v3
	v_mov_b32_e32 v33, v3
	v_mov_b32_e32 v34, v3
	s_waitcnt lgkmcnt(0)
	s_nop 1
	v_add_f32_dpp v2, v2, v2 quad_perm:[1,0,3,2] row_mask:0xf bank_mask:0xf
	v_mov_b32_e32 v35, v3
	s_waitcnt lgkmcnt(0)
	s_nop 1
	v_add_f32_dpp v2, v2, v2 quad_perm:[2,3,0,1] row_mask:0xf bank_mask:0xf
	s_waitcnt lgkmcnt(0)
	s_nop 1
	v_add_f32_dpp v2, v2, v2 row_half_mirror row_mask:0xf bank_mask:0xf
	s_waitcnt lgkmcnt(0)
	s_nop 1
	v_add_f32_dpp v2, v2, v2 row_ror:8 row_mask:0xf bank_mask:0xf
	s_waitcnt lgkmcnt(0)
	v_mov_b32_e32 v22, v2
	s_nop 1
	v_permlane16_swap_b32_e32 v22, v2
	v_add_f32_e32 v2, v2, v22
	v_lshl_add_u64 v[22:23], v[16:17], 0, s[72:73]
	s_waitcnt lgkmcnt(0)
	v_mov_b32_e32 v27, v2
	s_nop 1
	v_permlane32_swap_b32_e32 v27, v2
	v_add_f32_e32 v2, v2, v27
	v_fmamk_f32 v2, v2, 0x3a800000, v220
	v_mul_f32_e32 v27, 0x4f800000, v2
	v_cmp_gt_f32_e32 vcc, s93, v2
	s_nop 1
	v_cndmask_b32_e32 v2, v2, v27, vcc
	v_sqrt_f32_e32 v27, v2
	s_nop 0
	v_add_u32_e32 v46, -1, v27
	v_add_u32_e32 v47, 1, v27
	v_fma_f32 v54, -v46, v27, v2
	v_fma_f32 v55, -v47, v27, v2
	v_cmp_ge_f32_e64 s[0:1], 0, v54
	s_nop 1
	v_cndmask_b32_e64 v27, v27, v46, s[0:1]
	v_cmp_lt_f32_e64 s[0:1], 0, v55
	s_nop 1
	v_cndmask_b32_e64 v27, v27, v47, s[0:1]
	v_mul_f32_e32 v46, 0x37800000, v27
	v_cndmask_b32_e32 v27, v27, v46, vcc
	v_cmp_class_f32_e32 vcc, v2, v221
	s_nop 1
	v_cndmask_b32_e32 v2, v27, v2, vcc
	v_div_scale_f32 v46, s[0:1], v2, v2, 1.0
	v_rcp_f32_e32 v47, v46
	v_mov_b32_e32 v27, v31
	v_div_scale_f32 v31, vcc, 1.0, v2, 1.0
	v_fma_f32 v54, -v46, v47, 1.0
	v_fmac_f32_e32 v47, v54, v47
	v_mul_f32_e32 v54, v31, v47
	v_fma_f32 v55, -v46, v54, v31
	v_fmac_f32_e32 v54, v55, v47
	v_fma_f32 v31, -v46, v54, v31
	v_div_fmas_f32 v31, v31, v47, v54
	v_div_fixup_f32 v2, v31, v2, 1.0
	v_pk_mul_f32 v[44:45], v[2:3], v[44:45] op_sel_hi:[0,1]
	v_pk_mul_f32 v[52:53], v[2:3], v[52:53] op_sel_hi:[0,1]
	v_pk_mul_f32 v[48:49], v[2:3], v[48:49] op_sel_hi:[0,1]
	v_pk_mul_f32 v[26:27], v[26:27], v[2:3] op_sel_hi:[1,0]
	v_pk_mul_f32 v[44:45], v[36:37], v[44:45]
	v_pk_mul_f32 v[52:53], v[12:13], v[52:53]
	v_pk_mul_f32 v[48:49], v[8:9], v[48:49]
	v_pk_mul_f32 v[26:27], v[4:5], v[26:27]
	v_cvt_pk_fp8_f32 v32, v44, v45
	v_cvt_pk_fp8_f32 v33, v52, v53
	v_cvt_pk_fp8_f32 v34, v48, v49
	v_cvt_pk_fp8_f32 v35, v26, v27
	v_pk_mul_f32 v[40:41], v[2:3], v[40:41] op_sel_hi:[0,1]
	v_pk_mul_f32 v[42:43], v[2:3], v[42:43] op_sel_hi:[0,1]
	v_pk_mul_f32 v[50:51], v[2:3], v[50:51] op_sel_hi:[0,1]
	v_pk_mul_f32 v[28:29], v[28:29], v[2:3] op_sel_hi:[1,0]
	v_pk_mul_f32 v[40:41], v[38:39], v[40:41]
	v_pk_mul_f32 v[42:43], v[14:15], v[42:43]
	v_pk_mul_f32 v[50:51], v[10:11], v[50:51]
	v_pk_mul_f32 v[28:29], v[6:7], v[28:29]
	v_cvt_pk_fp8_f32 v32, v40, v41 op_sel:[0,0,1]
	v_cvt_pk_fp8_f32 v33, v42, v43 op_sel:[0,0,1]
	v_cvt_pk_fp8_f32 v34, v50, v51 op_sel:[0,0,1]
	v_cvt_pk_fp8_f32 v35, v28, v29 op_sel:[0,0,1]
	v_add_co_u32_e32 v46, vcc, 0x48000000, v22
	v_add_u32_e32 v26, s2, v30
	s_nop 0
	v_addc_co_u32_e32 v47, vcc, 0, v23, vcc
	global_store_dwordx4 v[46:47], v[32:35], off
	s_and_saveexec_b64 s[0:1], s[6:7]
	s_cbranch_execz .LBB0_1759
	v_add_u32_e32 v2, 0x22680, v26
	ds_read_b32 v2, v2
	s_waitcnt lgkmcnt(0)
	v_bfe_u32 v27, v2, 16, 16
	v_and_b32_e32 v2, 0xffff, v2
	v_lshl_add_u32 v2, v27, 14, v2
	v_lshl_add_u64 v[28:29], v[2:3], 2, s[4:5]
	v_mov_b32_e32 v2, s8
	global_store_dword v[28:29], v2, off
.LBB0_1759:
	s_or_b64 exec, exec, s[0:1]
	v_mov_b64_e32 v[32:33], v[128:129]
	v_mov_b64_e32 v[34:35], v[130:131]
	v_mov_b64_e32 v[40:41], v[132:133]
	v_mov_b64_e32 v[42:43], v[134:135]
	v_lshlrev_b32_e32 v48, 16, v32
	v_lshlrev_b32_e32 v44, 16, v40
	v_and_b32_e32 v45, 0xffff0000, v40
	v_lshlrev_b32_e32 v40, 16, v41
	v_and_b32_e32 v41, 0xffff0000, v41
	v_lshlrev_b32_e32 v47, 16, v43
	v_lshlrev_b32_e32 v46, 16, v42
	v_and_b32_e32 v43, 0xffff0000, v43
	v_and_b32_e32 v42, 0xffff0000, v42
	v_and_b32_e32 v49, 0xffff0000, v32
	v_mul_f32_e32 v2, v44, v44
	v_mul_f32_e32 v32, v40, v40
	v_lshlrev_b32_e32 v24, 16, v34
	v_and_b32_e32 v27, 0xffff0000, v34
	v_lshlrev_b32_e32 v28, 16, v35
	v_and_b32_e32 v29, 0xffff0000, v35
	v_lshlrev_b32_e32 v50, 16, v33
	v_and_b32_e32 v51, 0xffff0000, v33
	v_pk_mul_f32 v[34:35], v[42:43], v[42:43]
	v_pk_fma_f32 v[58:59], v[44:45], v[44:45], v[2:3] op_sel_hi:[1,1,0]
	v_pk_fma_f32 v[32:33], v[40:41], v[40:41], v[32:33] op_sel_hi:[1,1,0]
	v_mul_f32_e32 v52, v48, v48
	v_mul_f32_e32 v54, v50, v50
	v_mov_b32_e32 v56, v24
	v_pk_fma_f32 v[34:35], v[46:47], v[46:47], v[34:35]
	v_mov_b32_e32 v25, v59
	v_mov_b32_e32 v57, v33
	v_pk_fma_f32 v[52:53], v[48:49], v[48:49], v[52:53] op_sel_hi:[1,1,0]
	v_pk_fma_f32 v[54:55], v[50:51], v[50:51], v[54:55] op_sel_hi:[1,1,0]
	v_pk_add_f32 v[34:35], v[34:35], v[34:35] op_sel_hi:[0,1]
	v_pk_add_f32 v[32:33], v[58:59], v[32:33]
	v_pk_mul_f32 v[56:57], v[24:25], v[56:57]
	v_mul_f32_e32 v52, v28, v28
	v_mul_f32_e32 v54, v29, v29
	v_mul_f32_e32 v34, v27, v27
	v_mov_b32_e32 v57, v33
	v_pk_add_f32 v[52:53], v[52:53], v[54:55]
	v_pk_add_f32 v[32:33], v[56:57], v[34:35]
	v_mov_b32_e32 v34, v3
	v_pk_add_f32 v[32:33], v[32:33], v[52:53]
	v_mov_b32_e32 v52, v46
	v_add_f32_e32 v2, v32, v33
	v_mov_b32_e32 v53, v42
	v_mov_b32_e32 v42, v47
	v_mov_b32_e32 v32, v3
	v_mov_b32_e32 v33, v3
	s_waitcnt lgkmcnt(0)
	s_nop 1
	v_add_f32_dpp v2, v2, v2 quad_perm:[1,0,3,2] row_mask:0xf bank_mask:0xf
	v_mov_b32_e32 v35, v3
	s_waitcnt lgkmcnt(0)
	s_nop 1
	v_add_f32_dpp v2, v2, v2 quad_perm:[2,3,0,1] row_mask:0xf bank_mask:0xf
	s_waitcnt lgkmcnt(0)
	s_nop 1
	v_add_f32_dpp v2, v2, v2 row_half_mirror row_mask:0xf bank_mask:0xf
	s_waitcnt lgkmcnt(0)
	s_nop 1
	v_add_f32_dpp v2, v2, v2 row_ror:8 row_mask:0xf bank_mask:0xf
	s_waitcnt lgkmcnt(0)
	v_mov_b32_e32 v25, v2
	s_nop 1
	v_permlane16_swap_b32_e32 v25, v2
	v_add_f32_e32 v2, v2, v25
	s_waitcnt lgkmcnt(0)
	v_mov_b32_e32 v25, v2
	s_nop 1
	v_permlane32_swap_b32_e32 v25, v2
	v_add_f32_e32 v2, v2, v25
	v_fmamk_f32 v2, v2, 0x3a800000, v220
	v_mul_f32_e32 v25, 0x4f800000, v2
	v_cmp_gt_f32_e32 vcc, s93, v2
	s_nop 1
	v_cndmask_b32_e32 v2, v2, v25, vcc
	v_sqrt_f32_e32 v25, v2
	s_nop 0
	v_add_u32_e32 v31, -1, v25
	v_add_u32_e32 v46, 1, v25
	v_fma_f32 v47, -v31, v25, v2
	v_fma_f32 v54, -v46, v25, v2
	v_cmp_ge_f32_e64 s[0:1], 0, v47
	s_nop 1
	v_cndmask_b32_e64 v25, v25, v31, s[0:1]
	v_cmp_lt_f32_e64 s[0:1], 0, v54
	s_nop 1
	v_cndmask_b32_e64 v25, v25, v46, s[0:1]
	v_mul_f32_e32 v31, 0x37800000, v25
	v_cndmask_b32_e32 v25, v25, v31, vcc
	v_cmp_class_f32_e32 vcc, v2, v221
	s_nop 1
	v_cndmask_b32_e32 v2, v25, v2, vcc
	v_div_scale_f32 v31, s[0:1], v2, v2, 1.0
	v_rcp_f32_e32 v46, v31
	v_mov_b32_e32 v25, v27
	v_div_scale_f32 v27, vcc, 1.0, v2, 1.0
	v_fma_f32 v47, -v31, v46, 1.0
	v_fmac_f32_e32 v46, v47, v46
	v_mul_f32_e32 v47, v27, v46
	v_fma_f32 v54, -v31, v47, v27
	v_fmac_f32_e32 v47, v54, v46
	v_fma_f32 v27, -v31, v47, v27
	v_div_fmas_f32 v27, v27, v46, v47
	v_div_fixup_f32 v2, v27, v2, 1.0
	v_pk_mul_f32 v[44:45], v[2:3], v[44:45] op_sel_hi:[0,1]
	v_pk_mul_f32 v[46:47], v[2:3], v[52:53] op_sel_hi:[0,1]
	v_pk_mul_f32 v[48:49], v[2:3], v[48:49] op_sel_hi:[0,1]
	v_pk_mul_f32 v[24:25], v[24:25], v[2:3] op_sel_hi:[1,0]
	v_pk_mul_f32 v[44:45], v[36:37], v[44:45]
	v_pk_mul_f32 v[46:47], v[12:13], v[46:47]
	v_pk_mul_f32 v[48:49], v[8:9], v[48:49]
	v_pk_mul_f32 v[24:25], v[4:5], v[24:25]
	v_cvt_pk_fp8_f32 v32, v44, v45
	v_cvt_pk_fp8_f32 v33, v46, v47
	v_cvt_pk_fp8_f32 v34, v48, v49
	v_cvt_pk_fp8_f32 v35, v24, v25
	v_pk_mul_f32 v[40:41], v[2:3], v[40:41] op_sel_hi:[0,1]
	v_pk_mul_f32 v[42:43], v[2:3], v[42:43] op_sel_hi:[0,1]
	v_pk_mul_f32 v[50:51], v[2:3], v[50:51] op_sel_hi:[0,1]
	v_pk_mul_f32 v[28:29], v[28:29], v[2:3] op_sel_hi:[1,0]
	v_pk_mul_f32 v[40:41], v[38:39], v[40:41]
	v_pk_mul_f32 v[42:43], v[14:15], v[42:43]
	v_pk_mul_f32 v[50:51], v[10:11], v[50:51]
	v_pk_mul_f32 v[28:29], v[6:7], v[28:29]
	v_cvt_pk_fp8_f32 v32, v40, v41 op_sel:[0,0,1]
	v_cvt_pk_fp8_f32 v33, v42, v43 op_sel:[0,0,1]
	v_cvt_pk_fp8_f32 v34, v50, v51 op_sel:[0,0,1]
	v_cvt_pk_fp8_f32 v35, v28, v29 op_sel:[0,0,1]
	v_add_co_u32_e32 v22, vcc, 0x48000000, v22
	s_nop 1
	v_addc_co_u32_e32 v23, vcc, 0, v23, vcc
	global_store_dwordx4 v[22:23], v[32:35], off offset:1024
	s_and_saveexec_b64 s[0:1], s[6:7]
	s_cbranch_execz .LBB0_1756
	v_add_u32_e32 v2, 0x22690, v26
	ds_read_b32 v2, v2
	s_add_i32 s3, s8, 1
	s_waitcnt lgkmcnt(0)
	v_bfe_u32 v22, v2, 16, 16
	v_and_b32_e32 v2, 0xffff, v2
	v_lshl_add_u32 v2, v22, 14, v2
	v_lshl_add_u64 v[22:23], v[2:3], 2, s[4:5]
	v_mov_b32_e32 v2, s3
	global_store_dword v[22:23], v2, off
	s_branch .LBB0_1756

.LBB0_2041:
	v_mov_b32_e32 v2, v0
	s_lshl_b32 s8, s8, 3
	v_readfirstlane_b32 s9, v2
	s_ashr_i32 s9, s9, 6
	s_add_i32 s22, s9, s8
	s_cmpk_gt_i32 s22, 0x3fff
	s_cbranch_scc1 .LBB0_2057
	v_readlane_b32 s12, v254, 15
	v_readlane_b32 s14, v254, 17
	v_readlane_b32 s15, v254, 18
	s_add_u32 s8, s14, s3
	s_addc_u32 s9, s15, 0
	s_lshl_b32 s28, s2, 3
	v_readlane_b32 s13, v254, 16
	s_and_b64 s[6:7], s[6:7], exec
	s_cselect_b32 s7, s13, 0
	s_cselect_b32 s6, s12, 0
	s_cmp_lg_u64 s[6:7], 0
	s_cselect_b64 s[16:17], -1, 0
	s_add_u32 s29, s8, 0x1f00000
	s_addc_u32 s30, s9, 0
	s_add_u32 s31, s8, 0x1f80000
	s_addc_u32 s34, s9, 0
	s_add_i32 s3, s22, s28
	s_cmpk_lt_i32 s3, 0x4000
	s_cselect_b32 s10, s3, s22
	s_ashr_i32 s11, s10, 31
	s_lshl_b64 s[10:11], s[10:11], 4
	s_add_u32 s12, s31, s10
	s_addc_u32 s13, s34, s11
	s_ashr_i32 s23, s22, 31
	s_lshl_b64 s[14:15], s[22:23], 4
	s_add_u32 s18, s31, s14
	s_addc_u32 s19, s34, s15
	s_add_u32 s10, s29, s10
	s_addc_u32 s11, s30, s11
	global_load_dwordx4 v[8:11], v3, s[10:11]
	s_add_u32 s10, s29, s14
	s_addc_u32 s11, s30, s15
	global_load_dwordx4 v[20:23], v3, s[10:11]
	global_load_dwordx4 v[12:15], v3, s[12:13]
	global_load_dwordx4 v[4:7], v3, s[18:19]
	v_and_b32_e32 v26, 63, v2
	v_lshlrev_b32_e32 v2, 5, v26
	v_lshl_add_u64 v[16:17], s[0:1], 0, v[2:3]
	v_lshl_add_u64 v[44:45], s[6:7], 0, v[2:3]
	v_lshlrev_b32_e32 v2, 4, v26
	v_lshl_add_u64 v[24:25], s[8:9], 0, v[2:3]
	v_lshlrev_b32_e32 v2, 3, v26
	s_mov_b64 s[6:7], 0xc9000000
	v_lshl_add_u64 v[46:47], v[24:25], 0, s[6:7]
	v_lshl_add_u64 v[24:25], s[8:9], 0, v[2:3]
	s_mov_b64 s[6:7], 0x88000000
	v_lshl_add_u64 v[48:49], v[24:25], 0, s[6:7]
	s_mov_b64 s[6:7], 0x2000000
	s_cmp_lg_u64 s[0:1], 0
	v_lshl_add_u64 v[50:51], v[24:25], 0, s[6:7]
	s_cselect_b64 s[18:19], -1, 0
	s_cbranch_scc0 .Lcmb_nogain
	global_load_dwordx4 v[128:131], v[16:17], off
	global_load_dwordx4 v[132:135], v[16:17], off offset:16
	global_load_dwordx4 v[136:139], v[16:17], off offset:2048
	global_load_dwordx4 v[140:143], v[16:17], off offset:2064
.Lcmb_nogain:
	s_lshl_b32 s35, s2, 4
	s_mul_i32 s36, s2, 24
	s_waitcnt vmcnt(3)
	v_readfirstlane_b32 s12, v8
	v_readfirstlane_b32 s13, v9
	v_readfirstlane_b32 s14, v10
	v_readfirstlane_b32 s15, v11
	s_waitcnt vmcnt(2)
	v_readfirstlane_b32 s8, v20
	v_readfirstlane_b32 s9, v21
	v_readfirstlane_b32 s10, v22
	v_readfirstlane_b32 s11, v23
	s_branch .LBB0_2044

.LBB0_2047:
	v_cndmask_b32_e64 v2, 0, 1, s[18:19]
	v_cmp_ne_u32_e64 s[6:7], 1, v2
	s_andn2_b64 vcc, exec, s[18:19]
	s_cbranch_vccnz .LBB0_2049
	v_pk_mul_f32 v[70:71], v[36:37], v[36:37]
	v_pk_mul_f32 v[72:73], v[38:39], v[38:39]
	v_add_f32_e32 v2, v70, v71
	v_add_f32_e32 v2, v2, v72
	v_pk_mul_f32 v[74:75], v[40:41], v[40:41]
	v_add_f32_e32 v2, v73, v2
	v_add_f32_e32 v2, v74, v2
	v_pk_mul_f32 v[76:77], v[42:43], v[42:43]
	v_add_f32_e32 v2, v75, v2
	v_add_f32_e32 v2, v76, v2
	v_pk_mul_f32 v[78:79], v[28:29], v[28:29]
	v_add_f32_e32 v2, v77, v2
	v_add_f32_e32 v2, v78, v2
	v_pk_mul_f32 v[80:81], v[30:31], v[30:31]
	v_add_f32_e32 v2, v79, v2
	v_add_f32_e32 v2, v80, v2
	v_pk_mul_f32 v[82:83], v[32:33], v[32:33]
	v_add_f32_e32 v2, v81, v2
	v_add_f32_e32 v2, v82, v2
	v_pk_mul_f32 v[84:85], v[34:35], v[34:35]
	v_add_f32_e32 v2, v83, v2
	v_add_f32_e32 v2, v84, v2
	v_add_f32_e32 v2, v85, v2
	s_waitcnt lgkmcnt(0)
	s_nop 1
	v_add_f32_dpp v2, v2, v2 quad_perm:[1,0,3,2] row_mask:0xf bank_mask:0xf
	s_waitcnt lgkmcnt(0)
	s_nop 1
	v_add_f32_dpp v2, v2, v2 quad_perm:[2,3,0,1] row_mask:0xf bank_mask:0xf
	s_waitcnt lgkmcnt(0)
	s_nop 1
	v_add_f32_dpp v2, v2, v2 row_half_mirror row_mask:0xf bank_mask:0xf
	s_waitcnt lgkmcnt(0)
	s_nop 1
	v_add_f32_dpp v2, v2, v2 row_ror:8 row_mask:0xf bank_mask:0xf
	s_waitcnt lgkmcnt(0)
	v_mov_b32_e32 v70, v2
	s_nop 1
	v_permlane16_swap_b32_e32 v70, v2
	v_add_f32_e32 v2, v2, v70
	s_waitcnt lgkmcnt(0)
	v_mov_b32_e32 v70, v2
	s_nop 1
	v_permlane32_swap_b32_e32 v70, v2
	v_add_f32_e32 v2, v2, v70
	v_fmamk_f32 v2, v2, 0x3a800000, v220
	v_cmp_gt_f32_e32 vcc, s93, v2
	v_mul_f32_e32 v70, 0x4f800000, v2
	s_nop 0
	v_cndmask_b32_e32 v2, v2, v70, vcc
	v_sqrt_f32_e32 v70, v2
	s_nop 0
	v_add_u32_e32 v71, -1, v70
	v_fma_f32 v72, -v71, v70, v2
	v_cmp_ge_f32_e64 s[0:1], 0, v72
	v_add_u32_e32 v72, 1, v70
	s_nop 0
	v_cndmask_b32_e64 v71, v70, v71, s[0:1]
	v_fma_f32 v70, -v72, v70, v2
	v_cmp_lt_f32_e64 s[0:1], 0, v70
	s_nop 1
	v_cndmask_b32_e64 v70, v71, v72, s[0:1]
	v_mul_f32_e32 v71, 0x37800000, v70
	v_cndmask_b32_e32 v70, v70, v71, vcc
	v_cmp_class_f32_e32 vcc, v2, v221
	s_nop 1
	v_cndmask_b32_e32 v2, v70, v2, vcc
	v_div_scale_f32 v70, s[0:1], v2, v2, 1.0
	v_rcp_f32_e32 v71, v70
	s_lshl_b64 s[0:1], s[22:23], 10
	v_fma_f32 v72, -v70, v71, 1.0
	v_fmac_f32_e32 v71, v72, v71
	v_div_scale_f32 v72, vcc, 1.0, v2, 1.0
	v_mul_f32_e32 v73, v72, v71
	v_fma_f32 v74, -v70, v73, v72
	v_fmac_f32_e32 v73, v74, v71
	v_fma_f32 v70, -v70, v73, v72
	v_div_fmas_f32 v70, v70, v71, v73
	v_div_fixup_f32 v2, v70, v2, 1.0
	v_mul_f32_e32 v36, v36, v2
	v_mul_f32_e32 v28, v28, v2
	v_mul_f32_e32 v74, v128, v36
	v_mul_f32_e32 v36, v37, v2
	v_mul_f32_e32 v75, v129, v36
	v_mul_f32_e32 v36, v38, v2
	v_mul_f32_e32 v76, v130, v36
	v_mul_f32_e32 v36, v39, v2
	v_mul_f32_e32 v77, v131, v36
	v_mul_f32_e32 v36, v40, v2
	v_mul_f32_e32 v70, v132, v36
	v_mul_f32_e32 v36, v41, v2
	v_mul_f32_e32 v71, v133, v36
	v_mul_f32_e32 v36, v42, v2
	v_mul_f32_e32 v72, v134, v36
	v_mul_f32_e32 v36, v43, v2
	v_mul_f32_e32 v73, v135, v36
	v_mul_f32_e32 v40, v136, v28
	v_mul_f32_e32 v28, v29, v2
	v_mul_f32_e32 v41, v137, v28
	v_mul_f32_e32 v28, v30, v2
	v_mul_f32_e32 v42, v138, v28
	v_mul_f32_e32 v28, v31, v2
	v_mul_f32_e32 v43, v139, v28
	v_mul_f32_e32 v28, v32, v2
	v_mul_f32_e32 v32, v140, v28
	v_mul_f32_e32 v28, v33, v2
	v_mul_f32_e32 v33, v141, v28
	v_mul_f32_e32 v28, v34, v2
	v_mul_f32_e32 v34, v142, v28
	v_mov_b32_e32 v28, v3
	v_mov_b32_e32 v29, v3
	v_cvt_pk_fp8_f32 v28, v74, v75
	v_cvt_pk_fp8_f32 v29, v70, v71
	v_lshl_add_u64 v[30:31], v[50:51], 0, s[0:1]
	v_mul_f32_e32 v2, v35, v2
	v_cvt_pk_fp8_f32 v28, v76, v77 op_sel:[0,0,1]
	v_cvt_pk_fp8_f32 v29, v72, v73 op_sel:[0,0,1]
	v_mul_f32_e32 v2, v143, v2
	global_store_dwordx2 v[30:31], v[28:29], off
	v_mov_b32_e32 v28, v3
	v_mov_b32_e32 v29, v3
	v_cvt_pk_fp8_f32 v28, v40, v41
	v_cvt_pk_fp8_f32 v29, v32, v33
	v_cvt_pk_fp8_f32 v28, v42, v43 op_sel:[0,0,1]
	v_cvt_pk_fp8_f32 v29, v34, v2 op_sel:[0,0,1]
	global_store_dwordx2 v[30:31], v[28:29], off offset:512

.LBB0_2053:
	s_and_b64 vcc, exec, s[6:7]
	s_cbranch_vccnz .LBB0_2043
	v_pk_mul_f32 v[32:33], v[28:29], v[28:29]
	v_pk_mul_f32 v[34:35], v[30:31], v[30:31]
	v_add_f32_e32 v2, v32, v33
	v_add_f32_e32 v2, v2, v34
	v_pk_mul_f32 v[36:37], v[24:25], v[24:25]
	v_add_f32_e32 v2, v35, v2
	v_add_f32_e32 v2, v36, v2
	v_pk_mul_f32 v[38:39], v[26:27], v[26:27]
	v_add_f32_e32 v2, v37, v2
	v_add_f32_e32 v2, v38, v2
	v_pk_mul_f32 v[40:41], v[12:13], v[12:13]
	v_add_f32_e32 v2, v39, v2
	v_add_f32_e32 v2, v40, v2
	v_pk_mul_f32 v[42:43], v[14:15], v[14:15]
	v_add_f32_e32 v2, v41, v2
	v_add_f32_e32 v2, v42, v2
	v_pk_mul_f32 v[52:53], v[20:21], v[20:21]
	v_add_f32_e32 v2, v43, v2
	v_add_f32_e32 v2, v52, v2
	v_pk_mul_f32 v[54:55], v[22:23], v[22:23]
	v_add_f32_e32 v2, v53, v2
	v_add_f32_e32 v2, v54, v2
	v_add_f32_e32 v2, v55, v2
	s_ashr_i32 s21, s20, 31
	s_waitcnt lgkmcnt(0)
	s_nop 1
	v_add_f32_dpp v2, v2, v2 quad_perm:[1,0,3,2] row_mask:0xf bank_mask:0xf
	s_waitcnt lgkmcnt(0)
	s_nop 1
	v_add_f32_dpp v2, v2, v2 quad_perm:[2,3,0,1] row_mask:0xf bank_mask:0xf
	s_waitcnt lgkmcnt(0)
	s_nop 1
	v_add_f32_dpp v2, v2, v2 row_half_mirror row_mask:0xf bank_mask:0xf
	s_waitcnt lgkmcnt(0)
	s_nop 1
	v_add_f32_dpp v2, v2, v2 row_ror:8 row_mask:0xf bank_mask:0xf
	s_waitcnt lgkmcnt(0)
	v_mov_b32_e32 v32, v2
	s_nop 1
	v_permlane16_swap_b32_e32 v32, v2
	v_add_f32_e32 v2, v2, v32
	s_waitcnt lgkmcnt(0)
	v_mov_b32_e32 v32, v2
	s_nop 1
	v_permlane32_swap_b32_e32 v32, v2
	v_add_f32_e32 v2, v2, v32
	v_fmamk_f32 v2, v2, 0x3a800000, v220
	v_cmp_gt_f32_e32 vcc, s93, v2
	v_mul_f32_e32 v32, 0x4f800000, v2
	s_nop 0
	v_cndmask_b32_e32 v2, v2, v32, vcc
	v_sqrt_f32_e32 v32, v2
	s_nop 0
	v_add_u32_e32 v33, -1, v32
	v_fma_f32 v34, -v33, v32, v2
	v_cmp_ge_f32_e64 s[0:1], 0, v34
	v_add_u32_e32 v34, 1, v32
	s_nop 0
	v_cndmask_b32_e64 v33, v32, v33, s[0:1]
	v_fma_f32 v32, -v34, v32, v2
	v_cmp_lt_f32_e64 s[0:1], 0, v32
	s_nop 1
	v_cndmask_b32_e64 v32, v33, v34, s[0:1]
	v_mul_f32_e32 v33, 0x37800000, v32
	v_cndmask_b32_e32 v32, v32, v33, vcc
	v_cmp_class_f32_e32 vcc, v2, v221
	s_nop 1
	v_cndmask_b32_e32 v2, v32, v2, vcc
	v_div_scale_f32 v32, s[0:1], v2, v2, 1.0
	v_rcp_f32_e32 v33, v32
	s_lshl_b64 s[0:1], s[20:21], 10
	v_fma_f32 v34, -v32, v33, 1.0
	v_fmac_f32_e32 v33, v34, v33
	v_div_scale_f32 v34, vcc, 1.0, v2, 1.0
	v_mul_f32_e32 v35, v34, v33
	v_fma_f32 v36, -v32, v35, v34
	v_fmac_f32_e32 v35, v36, v33
	v_fma_f32 v32, -v32, v35, v34
	v_div_fmas_f32 v32, v32, v33, v35
	v_div_fixup_f32 v2, v32, v2, 1.0
	v_mul_f32_e32 v28, v28, v2
	v_mul_f32_e32 v24, v24, v2
	v_mul_f32_e32 v12, v12, v2
	v_mul_f32_e32 v32, v132, v24
	v_mul_f32_e32 v36, v128, v28
	v_mul_f32_e32 v28, v29, v2
	v_mul_f32_e32 v24, v25, v2
	v_mul_f32_e32 v37, v129, v28
	v_mul_f32_e32 v28, v30, v2
	v_mul_f32_e32 v33, v133, v24
	v_mul_f32_e32 v24, v26, v2
	v_mul_f32_e32 v38, v130, v28
	v_mul_f32_e32 v28, v31, v2
	v_mul_f32_e32 v34, v134, v24
	v_mul_f32_e32 v24, v27, v2
	v_mul_f32_e32 v39, v131, v28
	v_mul_f32_e32 v35, v135, v24
	v_mul_f32_e32 v28, v136, v12
	v_mul_f32_e32 v12, v13, v2
	v_mul_f32_e32 v29, v137, v12
	v_mul_f32_e32 v12, v14, v2
	v_mul_f32_e32 v30, v138, v12
	v_mul_f32_e32 v12, v15, v2
	v_mul_f32_e32 v31, v139, v12
	v_mul_f32_e32 v12, v20, v2
	v_mul_f32_e32 v20, v140, v12
	v_mul_f32_e32 v12, v21, v2
	v_mul_f32_e32 v21, v141, v12
	v_mul_f32_e32 v12, v22, v2
	v_mul_f32_e32 v22, v142, v12
	v_mov_b32_e32 v12, v3
	v_mov_b32_e32 v13, v3
	v_cvt_pk_fp8_f32 v12, v36, v37
	v_cvt_pk_fp8_f32 v13, v32, v33
	v_lshl_add_u64 v[14:15], v[50:51], 0, s[0:1]
	v_mul_f32_e32 v2, v23, v2
	v_cvt_pk_fp8_f32 v12, v38, v39 op_sel:[0,0,1]
	v_cvt_pk_fp8_f32 v13, v34, v35 op_sel:[0,0,1]
	v_mul_f32_e32 v2, v143, v2
	global_store_dwordx2 v[14:15], v[12:13], off
	v_mov_b32_e32 v12, v3
	v_mov_b32_e32 v13, v3
	v_cvt_pk_fp8_f32 v12, v28, v29
	v_cvt_pk_fp8_f32 v13, v20, v21
	v_cvt_pk_fp8_f32 v12, v30, v31 op_sel:[0,0,1]
	v_cvt_pk_fp8_f32 v13, v22, v2 op_sel:[0,0,1]
	global_store_dwordx2 v[14:15], v[12:13], off offset:512
	s_branch .LBB0_2043
